# v14 + sc0 sc1 (write-through) on every dwordx4 epilogue store of P0 part1/P2/P4/P5/P8 (less dirty L2 for the grid-barrier write-back)
# speedup vs baseline: 1.0017x; 1.0017x over previous
; #define LAS __attribute__((address_space(3)))
; #define LDS_WAIT() asm volatile("s_waitcnt lgkmcnt(0)" ::: "memory")
; __device__ __forceinline__ void p0_transpose_item(const float* W, int N, int k0, int n0, bf16_t* dst, int dK, bool rope_perm, LAS float* scr, int lane) {
; #pragma unroll 8
;     for (int i = 0; i < 32; ++i) { const int kk = 2 * i + (lane >> 5); scr[kk * 33 + (lane & 31)] = W[(size_t)(k0 + kk) * N + n0 + (lane & 31)]; }
;     LDS_WAIT(); asm volatile("" ::: "memory");
.LBB0_47:
	s_lshl_b32 s73, s69, 1
	s_lshl_b32 s74, s70, 1
	v_or_b32_e32 v27, s73, v1
	v_or_b32_e32 v60, s74, v4
	s_add_i32 s75, s73, 4
	s_add_i32 s76, s74, 4
	s_add_i32 s77, s73, 8
	s_add_i32 s78, s74, 8
	s_add_i32 s79, s73, 12
	s_add_i32 s84, s74, 12
	s_add_i32 s85, s73, 16
	s_add_i32 s86, s74, 16
	s_add_i32 s87, s73, 20
	s_add_i32 s88, s74, 20
	s_add_i32 s89, s73, 24
	s_add_i32 s90, s74, 24
	s_add_i32 s73, s73, 28
	s_add_i32 s74, s74, 28
	v_add_u32_e32 v28, s4, v60
	v_or_b32_e32 v61, s75, v1
	v_or_b32_e32 v62, s76, v4
	v_or_b32_e32 v63, s77, v1
	v_or_b32_e32 v64, s78, v4
	v_or_b32_e32 v65, s79, v1
	v_or_b32_e32 v66, s84, v4
	v_or_b32_e32 v67, s85, v1
	v_or_b32_e32 v68, s86, v4
	v_or_b32_e32 v69, s87, v1
	v_or_b32_e32 v70, s88, v4
	v_or_b32_e32 v71, s89, v1
	v_or_b32_e32 v72, s90, v4
	v_or_b32_e32 v73, s73, v1
	v_or_b32_e32 v74, s74, v4
	v_add_u32_e32 v30, s68, v27
	v_mad_i64_i32 v[28:29], s[74:75], v28, s43, v[20:21]
	v_add_u32_e32 v34, s68, v61
	v_add_u32_e32 v32, s4, v62
	v_add_u32_e32 v38, s68, v63
	v_add_u32_e32 v36, s4, v64
	v_add_u32_e32 v42, s68, v65
	v_add_u32_e32 v40, s4, v66
	v_add_u32_e32 v46, s68, v67
	v_add_u32_e32 v44, s4, v68
	v_add_u32_e32 v50, s68, v69
	v_add_u32_e32 v48, s4, v70
	v_add_u32_e32 v54, s68, v71
	v_add_u32_e32 v52, s4, v72
	v_add_u32_e32 v58, s68, v73
	v_add_u32_e32 v56, s4, v74
	v_mad_i64_i32 v[30:31], s[74:75], v30, s43, v[20:21]
	v_mad_i64_i32 v[32:33], s[74:75], v32, s43, v[20:21]
	v_mad_i64_i32 v[34:35], s[74:75], v34, s43, v[20:21]
	v_mad_i64_i32 v[36:37], s[74:75], v36, s43, v[20:21]
	v_mad_i64_i32 v[38:39], s[74:75], v38, s43, v[20:21]
	v_mad_i64_i32 v[40:41], s[74:75], v40, s43, v[20:21]
	v_mad_i64_i32 v[42:43], s[74:75], v42, s43, v[20:21]
	v_mad_i64_i32 v[44:45], s[74:75], v44, s43, v[20:21]
	v_mad_i64_i32 v[46:47], s[74:75], v46, s43, v[20:21]
	v_mad_i64_i32 v[48:49], s[74:75], v48, s43, v[20:21]
	v_mad_i64_i32 v[50:51], s[74:75], v50, s43, v[20:21]
	v_mad_i64_i32 v[52:53], s[74:75], v52, s43, v[20:21]
	v_mad_i64_i32 v[54:55], s[74:75], v54, s43, v[20:21]
	v_mad_i64_i32 v[56:57], s[74:75], v56, s43, v[20:21]
	v_mad_i64_i32 v[58:59], s[74:75], v58, s43, v[20:21]
	global_load_dword v75, v[28:29], off
	global_load_dword v76, v[30:31], off
	global_load_dword v77, v[32:33], off
	global_load_dword v78, v[34:35], off
	global_load_dword v79, v[36:37], off
	global_load_dword v80, v[38:39], off
	global_load_dword v81, v[40:41], off
	global_load_dword v82, v[42:43], off
	global_load_dword v83, v[44:45], off
	global_load_dword v84, v[46:47], off
	global_load_dword v85, v[48:49], off
	global_load_dword v86, v[50:51], off
	global_load_dword v87, v[52:53], off
	global_load_dword v88, v[54:55], off
	global_load_dword v89, v[56:57], off
	global_load_dword v90, v[58:59], off
	s_add_i32 s70, s70, 16
	s_add_i32 s69, s69, 16
	s_add_i32 s71, s71, -16
	v_mad_u64_u32 v[28:29], s[74:75], v60, s42, v[10:11]
	s_cmp_lg_u32 s71, 0
	v_mad_u64_u32 v[30:31], s[74:75], v27, s42, v[10:11]
	v_mad_u64_u32 v[32:33], s[74:75], v62, s42, v[10:11]
	v_mad_u64_u32 v[34:35], s[74:75], v61, s42, v[10:11]
	v_mad_u64_u32 v[36:37], s[74:75], v64, s42, v[10:11]
	v_mad_u64_u32 v[38:39], s[74:75], v63, s42, v[10:11]
	v_mad_u64_u32 v[40:41], s[74:75], v66, s42, v[10:11]
	v_mad_u64_u32 v[42:43], s[74:75], v65, s42, v[10:11]
	v_mad_u64_u32 v[44:45], s[74:75], v68, s42, v[10:11]
	v_mad_u64_u32 v[46:47], s[74:75], v67, s42, v[10:11]
	v_mad_u64_u32 v[48:49], s[74:75], v70, s42, v[10:11]
	v_mad_u64_u32 v[50:51], s[74:75], v69, s42, v[10:11]
	v_mad_u64_u32 v[52:53], s[74:75], v72, s42, v[10:11]
	v_mad_u64_u32 v[54:55], s[74:75], v71, s42, v[10:11]
	v_mad_u64_u32 v[56:57], s[74:75], v74, s42, v[10:11]
	v_mad_u64_u32 v[58:59], s[74:75], v73, s42, v[10:11]
	s_waitcnt vmcnt(15)
	ds_write_b32 v28, v75
	s_waitcnt vmcnt(14)
	ds_write_b32 v30, v76
	s_waitcnt vmcnt(13)
	ds_write_b32 v32, v77
	s_waitcnt vmcnt(12)
	ds_write_b32 v34, v78
	s_waitcnt vmcnt(11)
	ds_write_b32 v36, v79
	s_waitcnt vmcnt(10)
	ds_write_b32 v38, v80
	s_waitcnt vmcnt(9)
	ds_write_b32 v40, v81
	s_waitcnt vmcnt(8)
	ds_write_b32 v42, v82
	s_waitcnt vmcnt(7)
	ds_write_b32 v44, v83
	s_waitcnt vmcnt(6)
	ds_write_b32 v46, v84
	s_waitcnt vmcnt(5)
	ds_write_b32 v48, v85
	s_waitcnt vmcnt(4)
	ds_write_b32 v50, v86
	s_waitcnt vmcnt(3)
	ds_write_b32 v52, v87
	s_waitcnt vmcnt(2)
	ds_write_b32 v54, v88
	s_waitcnt vmcnt(1)
	ds_write_b32 v56, v89
	s_waitcnt vmcnt(0)
	ds_write_b32 v58, v90
	s_cbranch_scc1 .LBB0_47
; #define LAS __attribute__((address_space(3)))
; #define LDS_WAIT() asm volatile("s_waitcnt lgkmcnt(0)" ::: "memory")
; __device__ __forceinline__ unsigned pk2(float lo, float hi) { return f2bf(lo) | (f2bf(hi) << 16); }
; __device__ __forceinline__ void p0_transpose_item(const float* W, int N, int k0, int n0, bf16_t* dst, int dK, bool rope_perm, LAS float* scr, int lane) {
;     ...
;     const int c = lane & 7;
; #pragma unroll
;     for (int j = 0; j < 4; ++j) { const int n = (lane >> 3) + 8 * j; const int ns = rope_perm ? (16 * ((n >> 2) & 1) + 4 * (n >> 3) + (n & 3)) : n; const LAS float* s = scr + (8 * c) * 33 + ns;
;         u32x4 o; o.x = pk2(s[0 * 33], s[1 * 33]); o.y = pk2(s[2 * 33], s[3 * 33]); o.z = pk2(s[4 * 33], s[5 * 33]); o.w = pk2(s[6 * 33], s[7 * 33]);
;         *(u32x4*)(dst + (size_t)n * dK + k0 + 8 * c) = o; }
;     LDS_WAIT(); asm volatile("" ::: "memory");
	s_lshl_b64 s[38:39], s[38:39], 12
	s_add_u32 s70, s6, s38
	s_addc_u32 s71, s7, s39
	s_cmp_eq_u32 s5, 5
	s_cselect_b64 s[38:39], -1, 0
	s_cmp_eq_u32 s5, 2
	s_cselect_b64 s[68:69], -1, 0
	s_or_b64 vcc, s[68:69], s[38:39]
	s_waitcnt lgkmcnt(0)
	v_cndmask_b32_e32 v20, v2, v3, vcc
	v_lshl_add_u32 v27, v20, 2, v5
	ds_read2_b32 v[20:21], v27 offset1:33
	ds_read2_b32 v[30:31], v27 offset0:66 offset1:99
	ds_read2_b32 v[34:35], v27 offset0:198 offset1:231
	s_ashr_i32 s5, s4, 31
	s_lshl_b64 s[4:5], s[4:5], 1
	s_waitcnt lgkmcnt(2)
	v_bfe_u32 v28, v20, 16, 1
	v_add3_u32 v20, v20, v28, s44
	v_bfe_u32 v28, v21, 16, 1
	v_lshrrev_b32_e32 v20, 16, v20
	v_add3_u32 v21, v21, v28, s44
	v_and_or_b32 v28, v21, s45, v20
	s_waitcnt lgkmcnt(1)
	v_bfe_u32 v20, v30, 16, 1
	v_add3_u32 v29, v30, v20, s44
	ds_read2_b32 v[20:21], v27 offset0:132 offset1:165
	v_bfe_u32 v30, v31, 16, 1
	v_lshrrev_b32_e32 v29, 16, v29
	v_add3_u32 v30, v31, v30, s44
	v_and_or_b32 v29, v30, s45, v29
	s_waitcnt lgkmcnt(0)
	v_bfe_u32 v30, v20, 16, 1
	v_add3_u32 v20, v20, v30, s44
	v_bfe_u32 v27, v21, 16, 1
	v_lshrrev_b32_e32 v20, 16, v20
	v_add3_u32 v21, v21, v27, s44
	v_and_or_b32 v30, v21, s45, v20
	v_bfe_u32 v20, v34, 16, 1
	v_add3_u32 v20, v34, v20, s44
	v_lshrrev_b32_e32 v27, 16, v20
	v_cndmask_b32_e32 v20, v11, v22, vcc
	s_add_u32 s4, s70, s4
	v_lshl_add_u32 v36, v20, 2, v5
	s_addc_u32 s5, s71, s5
	v_bfe_u32 v31, v35, 16, 1
	ds_read2_b32 v[20:21], v36 offset1:33
	v_lshl_add_u64 v[32:33], s[4:5], 0, v[6:7]
	v_add3_u32 v31, v35, v31, s44
	v_and_or_b32 v31, v31, s45, v27
	v_lshl_add_u64 v[34:35], v[32:33], 0, v[12:13]
	global_store_dwordx4 v[34:35], v[28:31], off sc0 sc1
	ds_read2_b32 v[30:31], v36 offset0:66 offset1:99
	s_waitcnt lgkmcnt(1)
	v_bfe_u32 v27, v20, 16, 1
	v_add3_u32 v20, v20, v27, s44
	v_bfe_u32 v27, v21, 16, 1
	v_lshrrev_b32_e32 v20, 16, v20
	v_add3_u32 v21, v21, v27, s44
	v_and_or_b32 v28, v21, s45, v20
	s_waitcnt lgkmcnt(0)
	v_bfe_u32 v20, v30, 16, 1
	v_add3_u32 v27, v30, v20, s44
	ds_read2_b32 v[20:21], v36 offset0:132 offset1:165
	v_bfe_u32 v29, v31, 16, 1
	ds_read2_b32 v[34:35], v36 offset0:198 offset1:231
	v_lshrrev_b32_e32 v27, 16, v27
	v_add3_u32 v29, v31, v29, s44
	v_and_or_b32 v29, v29, s45, v27
	s_waitcnt lgkmcnt(1)
	v_bfe_u32 v27, v20, 16, 1
	v_add3_u32 v20, v20, v27, s44
	v_bfe_u32 v27, v21, 16, 1
	v_lshrrev_b32_e32 v20, 16, v20
	v_add3_u32 v21, v21, v27, s44
	v_and_or_b32 v30, v21, s45, v20
	s_waitcnt lgkmcnt(0)
	v_bfe_u32 v20, v34, 16, 1
	v_add3_u32 v20, v34, v20, s44
	v_lshrrev_b32_e32 v27, 16, v20
	v_cndmask_b32_e32 v20, v23, v24, vcc
	v_lshl_add_u32 v36, v20, 2, v5
	v_bfe_u32 v31, v35, 16, 1
	ds_read2_b32 v[20:21], v36 offset1:33
	v_add3_u32 v31, v35, v31, s44
	v_and_or_b32 v31, v31, s45, v27
	v_lshl_add_u64 v[34:35], v[32:33], 0, v[14:15]
	global_store_dwordx4 v[34:35], v[28:31], off sc0 sc1
	ds_read2_b32 v[30:31], v36 offset0:66 offset1:99
	s_waitcnt lgkmcnt(1)
	v_bfe_u32 v27, v20, 16, 1
	v_add3_u32 v20, v20, v27, s44
	v_bfe_u32 v27, v21, 16, 1
	v_lshrrev_b32_e32 v20, 16, v20
	v_add3_u32 v21, v21, v27, s44
	v_and_or_b32 v28, v21, s45, v20
	s_waitcnt lgkmcnt(0)
	v_bfe_u32 v20, v30, 16, 1
	v_add3_u32 v27, v30, v20, s44
	ds_read2_b32 v[20:21], v36 offset0:132 offset1:165
	v_bfe_u32 v29, v31, 16, 1
	ds_read2_b32 v[34:35], v36 offset0:198 offset1:231
	v_lshrrev_b32_e32 v27, 16, v27
	v_add3_u32 v29, v31, v29, s44
	v_and_or_b32 v29, v29, s45, v27
	s_waitcnt lgkmcnt(1)
	v_bfe_u32 v27, v20, 16, 1
	v_add3_u32 v20, v20, v27, s44
	v_bfe_u32 v27, v21, 16, 1
	v_lshrrev_b32_e32 v20, 16, v20
	v_add3_u32 v21, v21, v27, s44
	v_and_or_b32 v30, v21, s45, v20
	s_waitcnt lgkmcnt(0)
	v_bfe_u32 v20, v34, 16, 1
	v_add3_u32 v20, v34, v20, s44
	v_lshrrev_b32_e32 v27, 16, v20
	v_cndmask_b32_e32 v20, v25, v26, vcc
	v_lshl_add_u32 v36, v20, 2, v5
	v_bfe_u32 v31, v35, 16, 1
	ds_read2_b32 v[20:21], v36 offset1:33
	v_add3_u32 v31, v35, v31, s44
	v_and_or_b32 v31, v31, s45, v27
	v_lshl_add_u64 v[34:35], v[32:33], 0, v[16:17]
	global_store_dwordx4 v[34:35], v[28:31], off sc0 sc1
	ds_read2_b32 v[30:31], v36 offset0:66 offset1:99
	s_waitcnt lgkmcnt(1)
	v_bfe_u32 v27, v20, 16, 1
	v_add3_u32 v20, v20, v27, s44
	v_bfe_u32 v27, v21, 16, 1
	v_lshrrev_b32_e32 v20, 16, v20
	v_add3_u32 v21, v21, v27, s44
	v_and_or_b32 v28, v21, s45, v20
	s_waitcnt lgkmcnt(0)
	v_bfe_u32 v20, v30, 16, 1
	v_add3_u32 v27, v30, v20, s44
	ds_read2_b32 v[20:21], v36 offset0:132 offset1:165
	v_bfe_u32 v29, v31, 16, 1
	ds_read2_b32 v[34:35], v36 offset0:198 offset1:231
	v_lshrrev_b32_e32 v27, 16, v27
	v_add3_u32 v29, v31, v29, s44
	v_and_or_b32 v29, v29, s45, v27
	s_waitcnt lgkmcnt(1)
	v_bfe_u32 v27, v20, 16, 1
	v_add3_u32 v20, v20, v27, s44
	v_bfe_u32 v27, v21, 16, 1
	v_lshrrev_b32_e32 v20, 16, v20
	v_add3_u32 v21, v21, v27, s44
	v_and_or_b32 v30, v21, s45, v20
	s_waitcnt lgkmcnt(0)
	v_bfe_u32 v20, v34, 16, 1
	v_add3_u32 v20, v34, v20, s44
	v_bfe_u32 v21, v35, 16, 1
	v_lshrrev_b32_e32 v20, 16, v20
	v_add3_u32 v21, v35, v21, s44
	v_and_or_b32 v31, v21, s45, v20
	v_lshl_add_u64 v[20:21], v[32:33], 0, v[18:19]
	global_store_dwordx4 v[20:21], v[28:31], off sc0 sc1
	s_waitcnt lgkmcnt(0)
	s_branch .LBB0_44

; #define LAS __attribute__((address_space(3)))
; __device__ __forceinline__ unsigned cvt_pk_bf16(float lo, float hi) { unsigned r; asm volatile("v_cvt_pk_bf16_f32 %0, %1, %2" : "=v"(r) : "v"(lo), "v"(hi)); return r; }
;     __device__ __forceinline__ void operator()(const f32x4 (&acc)[2][2][4][2], const Unit& u, int wr, int wc, int fr, int fq) const {
;     ...
;                 for (int bj = 0; bj < 2; ++bj) {
;                     f32x4 v0 = acc[ai][bj][m][0], v1 = acc[ai][bj][m][1];
;                     if (do_rope) {
;                         const int pos = bj ? cpos : rpos;
;                         const f32x4* cs = (const f32x4*)(rope + pos * 16 + 4 * fq);
;                         const f32x4 c01 = cs[0], c23 = cs[1];
;                         const float cc[4] = {c01[0], c01[2], c23[0], c23[2]}, sn[4] = {c01[1], c01[3], c23[1], c23[3]};
;                         f32x4 o0, o1;
; #pragma unroll
;                         for (int e = 0; e < 4; ++e) { o0[e] = v0[e] * cc[e] - v1[e] * sn[e]; o1[e] = v1[e] * cc[e] + v0[e] * sn[e]; }
;                         v0 = o0; v1 = o1;
;                     }
;                     u32x4 w; w.x = cvt_pk_bf16(v0[0], v0[1]); w.y = cvt_pk_bf16(v0[2], v0[3]); w.z = cvt_pk_bf16(v1[0], v1[1]); w.w = cvt_pk_bf16(v1[2], v1[3]);
;                     *(LAS u32x4*)(my + fr * 144 + bj * 64 + fq * 16) = w;
;                 }
; #pragma unroll
;                 for (int hh = 0; hh < 2; ++hh) { const int row = (lane >> 3) + 8 * hh; const u32x4 x = *(const LAS u32x4*)(my + row * 144 + (lane & 7) * 16);
;                     *(u32x4*)(base + (size_t)(rowb + ai * 128 + wr * 64 + m * 16 + row) * ldc + colw) = x; }
.LBB0_288:
	s_add_i32 s6, s92, s76
	v_cvt_pk_bf16_f32 v118, v118, v119
	v_cvt_pk_bf16_f32 v119, v120, v121
	v_cvt_pk_bf16_f32 v120, v114, v115
	v_cvt_pk_bf16_f32 v121, v116, v117
	ds_write_b128 v180, v[118:121] offset:64
	ds_read_b128 v[114:117], v181
	v_add_u32_e32 v118, s6, v169
	v_add_u32_e32 v122, s93, v168
	v_ashrrev_i32_e32 v119, 31, v118
	v_ashrrev_i32_e32 v123, 31, v122
	v_mul_lo_u32 v120, s64, v119
	v_mul_lo_u32 v121, s65, v118
	v_mad_u64_u32 v[118:119], s[44:45], s64, v118, 0
	v_lshl_add_u64 v[122:123], v[122:123], 1, s[66:67]
	v_add3_u32 v119, v119, v120, v121
	v_lshl_add_u64 v[124:125], v[118:119], 1, v[122:123]
	ds_read_b128 v[118:121], v181 offset:1152
	s_waitcnt lgkmcnt(0)
	global_store_dwordx4 v[124:125], v[114:117], off sc0 sc1
	s_and_b64 vcc, exec, s[0:1]
	s_nop 0
	v_add_u32_e32 v114, s6, v172
	v_ashrrev_i32_e32 v115, 31, v114
	v_mul_lo_u32 v116, s64, v115
	v_mul_lo_u32 v117, s65, v114
	v_mad_u64_u32 v[114:115], s[44:45], s64, v114, 0
	v_add3_u32 v115, v115, v116, v117
	v_lshl_add_u64 v[114:115], v[114:115], 1, v[122:123]
	global_store_dwordx4 v[114:115], v[118:121], off sc0 sc1
	s_cbranch_vccnz .LBB0_290
	s_add_i32 s12, s84, s76
	s_lshl_b32 s12, s12, 1
	s_and_b32 s12, s12, 0x1f80
	v_lshl_add_u64 v[118:119], v[144:145], 0, s[12:13]
	global_load_dwordx4 v[114:117], v[118:119], off
	s_nop 0
	global_load_dwordx4 v[118:121], v[118:119], off offset:16
	s_waitcnt vmcnt(0)
	v_mov_b32_e32 v124, v114
	v_mul_f32_e32 v114, v112, v118
	v_mul_f32_e32 v126, v108, v119
	v_mul_f32_e32 v118, v108, v118
	v_mul_f32_e32 v128, v112, v119
	v_mov_b32_e32 v108, v113
	v_mov_b32_e32 v112, v109
	v_mov_b32_e32 v125, v116
	v_mov_b32_e32 v116, v115
	v_pk_mul_f32 v[108:109], v[108:109], v[120:121]
	v_pk_mul_f32 v[112:113], v[112:113], v[120:121]
	v_pk_mul_f32 v[158:159], v[106:107], v[116:117]
	v_pk_mul_f32 v[116:117], v[110:111], v[116:117]
	v_mov_b32_e32 v115, v108
	v_mov_b32_e32 v127, v109
	v_mov_b32_e32 v119, v112
	v_mov_b32_e32 v129, v113
	v_pk_fma_f32 v[110:111], v[110:111], v[124:125], v[158:159] neg_lo:[0,0,1] neg_hi:[0,0,1]
	v_pk_fma_f32 v[106:107], v[106:107], v[124:125], v[116:117]
	v_pk_add_f32 v[112:113], v[114:115], v[126:127] neg_lo:[0,1] neg_hi:[0,1]
	v_pk_add_f32 v[108:109], v[118:119], v[128:129]

; #define LAS __attribute__((address_space(3)))
; __device__ __forceinline__ unsigned cvt_pk_bf16(float lo, float hi) { unsigned r; asm volatile("v_cvt_pk_bf16_f32 %0, %1, %2" : "=v"(r) : "v"(lo), "v"(hi)); return r; }
;     __device__ __forceinline__ void operator()(const f32x4 (&acc)[2][2][4][2], const Unit& u, int wr, int wc, int fr, int fq) const {
;     ...
;                 for (int bj = 0; bj < 2; ++bj) {
;                     f32x4 v0 = acc[ai][bj][m][0], v1 = acc[ai][bj][m][1];
;                     if (do_rope) {
;                         const int pos = bj ? cpos : rpos;
;                         const f32x4* cs = (const f32x4*)(rope + pos * 16 + 4 * fq);
;                         const f32x4 c01 = cs[0], c23 = cs[1];
;                         const float cc[4] = {c01[0], c01[2], c23[0], c23[2]}, sn[4] = {c01[1], c01[3], c23[1], c23[3]};
;                         f32x4 o0, o1;
; #pragma unroll
;                         for (int e = 0; e < 4; ++e) { o0[e] = v0[e] * cc[e] - v1[e] * sn[e]; o1[e] = v1[e] * cc[e] + v0[e] * sn[e]; }
;                         v0 = o0; v1 = o1;
;                     }
;                     u32x4 w; w.x = cvt_pk_bf16(v0[0], v0[1]); w.y = cvt_pk_bf16(v0[2], v0[3]); w.z = cvt_pk_bf16(v1[0], v1[1]); w.w = cvt_pk_bf16(v1[2], v1[3]);
;                     *(LAS u32x4*)(my + fr * 144 + bj * 64 + fq * 16) = w;
;                 }
; #pragma unroll
;                 for (int hh = 0; hh < 2; ++hh) { const int row = (lane >> 3) + 8 * hh; const u32x4 x = *(const LAS u32x4*)(my + row * 144 + (lane & 7) * 16);
;                     *(u32x4*)(base + (size_t)(rowb + ai * 128 + wr * 64 + m * 16 + row) * ldc + colw) = x; }
.LBB0_292:
	v_cvt_pk_bf16_f32 v102, v102, v103
	v_cvt_pk_bf16_f32 v103, v104, v105
	v_cvt_pk_bf16_f32 v104, v98, v99
	s_nop 0
	v_cvt_pk_bf16_f32 v105, v100, v101
	ds_write_b128 v180, v[102:105] offset:64
	s_add_i32 s12, s6, 16
	ds_read_b128 v[98:101], v181
	v_add_u32_e32 v102, s12, v169
	v_ashrrev_i32_e32 v103, 31, v102
	v_mul_lo_u32 v104, s64, v103
	v_mul_lo_u32 v105, s65, v102
	v_mad_u64_u32 v[102:103], s[44:45], s64, v102, 0
	v_add3_u32 v103, v103, v104, v105
	v_lshl_add_u64 v[106:107], v[102:103], 1, v[122:123]
	ds_read_b128 v[102:105], v181 offset:1152
	s_waitcnt lgkmcnt(0)
	global_store_dwordx4 v[106:107], v[98:101], off sc0 sc1
	s_and_b64 vcc, exec, s[0:1]
	s_nop 0
	v_add_u32_e32 v98, s12, v172
	v_ashrrev_i32_e32 v99, 31, v98
	v_mul_lo_u32 v100, s64, v99
	v_mul_lo_u32 v101, s65, v98
	v_mad_u64_u32 v[98:99], s[44:45], s64, v98, 0
	v_add3_u32 v99, v99, v100, v101
	v_lshl_add_u64 v[98:99], v[98:99], 1, v[122:123]
	global_store_dwordx4 v[98:99], v[102:105], off sc0 sc1
	s_cbranch_vccnz .LBB0_294
	s_add_i32 s12, s84, s76
	s_lshl_b32 s12, s12, 1
	s_and_b32 s12, s12, 0x1f80
	v_lshl_add_u64 v[102:103], v[144:145], 0, s[12:13]
	global_load_dwordx4 v[98:101], v[102:103], off
	s_nop 0
	global_load_dwordx4 v[102:105], v[102:103], off offset:16
	s_waitcnt vmcnt(0)
	v_mov_b32_e32 v106, v98
	v_mul_f32_e32 v98, v96, v102
	v_mul_f32_e32 v108, v92, v103
	v_mul_f32_e32 v102, v92, v102
	v_mul_f32_e32 v110, v96, v103
	v_mov_b32_e32 v92, v97
	v_mov_b32_e32 v96, v93
	v_mov_b32_e32 v107, v100
	v_mov_b32_e32 v100, v99
	v_pk_mul_f32 v[92:93], v[92:93], v[104:105]
	v_pk_mul_f32 v[96:97], v[96:97], v[104:105]
	v_pk_mul_f32 v[112:113], v[90:91], v[100:101]
	v_pk_mul_f32 v[100:101], v[94:95], v[100:101]
	v_mov_b32_e32 v99, v92
	v_mov_b32_e32 v109, v93
	v_mov_b32_e32 v103, v96
	v_mov_b32_e32 v111, v97
	v_pk_fma_f32 v[94:95], v[94:95], v[106:107], v[112:113] neg_lo:[0,0,1] neg_hi:[0,0,1]
	v_pk_fma_f32 v[90:91], v[90:91], v[106:107], v[100:101]
	v_pk_add_f32 v[96:97], v[98:99], v[108:109] neg_lo:[0,1] neg_hi:[0,1]
	v_pk_add_f32 v[92:93], v[102:103], v[110:111]

; #define LAS __attribute__((address_space(3)))
; __device__ __forceinline__ unsigned cvt_pk_bf16(float lo, float hi) { unsigned r; asm volatile("v_cvt_pk_bf16_f32 %0, %1, %2" : "=v"(r) : "v"(lo), "v"(hi)); return r; }
;     __device__ __forceinline__ void operator()(const f32x4 (&acc)[2][2][4][2], const Unit& u, int wr, int wc, int fr, int fq) const {
;     ...
;             for (int m = 0; m < 4; ++m) {
;                 const int rl = ai * 128 + wr * 64 + m * 16 + fr;
;                 const int s = (lt * 256 + rl) & 4095, rpos = s >> 6, cpos = s & 63;
; #pragma unroll
;                 for (int bj = 0; bj < 2; ++bj) {
;                     f32x4 v0 = acc[ai][bj][m][0], v1 = acc[ai][bj][m][1];
;                     if (do_rope) {
;                         const int pos = bj ? cpos : rpos;
;                         const f32x4* cs = (const f32x4*)(rope + pos * 16 + 4 * fq);
;                         const f32x4 c01 = cs[0], c23 = cs[1];
;                         const float cc[4] = {c01[0], c01[2], c23[0], c23[2]}, sn[4] = {c01[1], c01[3], c23[1], c23[3]};
;                         f32x4 o0, o1;
; #pragma unroll
;                         for (int e = 0; e < 4; ++e) { o0[e] = v0[e] * cc[e] - v1[e] * sn[e]; o1[e] = v1[e] * cc[e] + v0[e] * sn[e]; }
;                         v0 = o0; v1 = o1;
;                     }
;                     u32x4 w; w.x = cvt_pk_bf16(v0[0], v0[1]); w.y = cvt_pk_bf16(v0[2], v0[3]); w.z = cvt_pk_bf16(v1[0], v1[1]); w.w = cvt_pk_bf16(v1[2], v1[3]);
;                     *(LAS u32x4*)(my + fr * 144 + bj * 64 + fq * 16) = w;
;                 }
; #pragma unroll
;                 for (int hh = 0; hh < 2; ++hh) { const int row = (lane >> 3) + 8 * hh; const u32x4 x = *(const LAS u32x4*)(my + row * 144 + (lane & 7) * 16);
;                     *(u32x4*)(base + (size_t)(rowb + ai * 128 + wr * 64 + m * 16 + row) * ldc + colw) = x; }
.LBB0_296:
	v_cvt_pk_bf16_f32 v86, v86, v87
	v_cvt_pk_bf16_f32 v87, v88, v89
	v_cvt_pk_bf16_f32 v88, v82, v83
	s_nop 0
	v_cvt_pk_bf16_f32 v89, v84, v85
	ds_write_b128 v180, v[86:89] offset:64
	s_add_i32 s12, s6, 32
	ds_read_b128 v[82:85], v181
	v_add_u32_e32 v86, s12, v169
	v_ashrrev_i32_e32 v87, 31, v86
	v_mul_lo_u32 v88, s64, v87
	v_mul_lo_u32 v89, s65, v86
	v_mad_u64_u32 v[86:87], s[44:45], s64, v86, 0
	v_add3_u32 v87, v87, v88, v89
	v_lshl_add_u64 v[90:91], v[86:87], 1, v[122:123]
	ds_read_b128 v[86:89], v181 offset:1152
	s_waitcnt lgkmcnt(0)
	global_store_dwordx4 v[90:91], v[82:85], off sc0 sc1
	s_and_b64 vcc, exec, s[0:1]
	s_nop 0
	v_add_u32_e32 v82, s12, v172
	v_ashrrev_i32_e32 v83, 31, v82
	v_mul_lo_u32 v84, s64, v83
	v_mul_lo_u32 v85, s65, v82
	v_mad_u64_u32 v[82:83], s[44:45], s64, v82, 0
	v_add3_u32 v83, v83, v84, v85
	v_lshl_add_u64 v[82:83], v[82:83], 1, v[122:123]
	global_store_dwordx4 v[82:83], v[86:89], off sc0 sc1
	s_cbranch_vccnz .LBB0_298
	s_add_i32 s12, s84, s76
	s_lshl_b32 s12, s12, 1
	s_and_b32 s12, s12, 0x1f80
	v_lshl_add_u64 v[86:87], v[144:145], 0, s[12:13]
	global_load_dwordx4 v[82:85], v[86:87], off
	s_nop 0
	global_load_dwordx4 v[86:89], v[86:87], off offset:16
	s_waitcnt vmcnt(0)
	v_mov_b32_e32 v90, v82
	v_mul_f32_e32 v82, v80, v86
	v_mul_f32_e32 v92, v76, v87
	v_mul_f32_e32 v86, v76, v86
	v_mul_f32_e32 v94, v80, v87
	v_mov_b32_e32 v76, v81
	v_mov_b32_e32 v80, v77
	v_mov_b32_e32 v91, v84
	v_mov_b32_e32 v84, v83
	v_pk_mul_f32 v[76:77], v[76:77], v[88:89]
	v_pk_mul_f32 v[80:81], v[80:81], v[88:89]
	v_pk_mul_f32 v[96:97], v[74:75], v[84:85]
	v_pk_mul_f32 v[84:85], v[78:79], v[84:85]
	v_mov_b32_e32 v83, v76
	v_mov_b32_e32 v93, v77
	v_mov_b32_e32 v87, v80
	v_mov_b32_e32 v95, v81
	v_pk_fma_f32 v[78:79], v[78:79], v[90:91], v[96:97] neg_lo:[0,0,1] neg_hi:[0,0,1]
	v_pk_fma_f32 v[74:75], v[74:75], v[90:91], v[84:85]
	v_pk_add_f32 v[80:81], v[82:83], v[92:93] neg_lo:[0,1] neg_hi:[0,1]
	v_pk_add_f32 v[76:77], v[86:87], v[94:95]

; #define LAS __attribute__((address_space(3)))
; __device__ __forceinline__ unsigned cvt_pk_bf16(float lo, float hi) { unsigned r; asm volatile("v_cvt_pk_bf16_f32 %0, %1, %2" : "=v"(r) : "v"(lo), "v"(hi)); return r; }
;     __device__ __forceinline__ void operator()(const f32x4 (&acc)[2][2][4][2], const Unit& u, int wr, int wc, int fr, int fq) const {
;     ...
;             for (int m = 0; m < 4; ++m) {
;                 const int rl = ai * 128 + wr * 64 + m * 16 + fr;
;                 const int s = (lt * 256 + rl) & 4095, rpos = s >> 6, cpos = s & 63;
; #pragma unroll
;                 for (int bj = 0; bj < 2; ++bj) {
;                     f32x4 v0 = acc[ai][bj][m][0], v1 = acc[ai][bj][m][1];
;                     if (do_rope) {
;                         const int pos = bj ? cpos : rpos;
;                         const f32x4* cs = (const f32x4*)(rope + pos * 16 + 4 * fq);
;                         const f32x4 c01 = cs[0], c23 = cs[1];
;                         const float cc[4] = {c01[0], c01[2], c23[0], c23[2]}, sn[4] = {c01[1], c01[3], c23[1], c23[3]};
;                         f32x4 o0, o1;
; #pragma unroll
;                         for (int e = 0; e < 4; ++e) { o0[e] = v0[e] * cc[e] - v1[e] * sn[e]; o1[e] = v1[e] * cc[e] + v0[e] * sn[e]; }
;                         v0 = o0; v1 = o1;
;                     }
;                     u32x4 w; w.x = cvt_pk_bf16(v0[0], v0[1]); w.y = cvt_pk_bf16(v0[2], v0[3]); w.z = cvt_pk_bf16(v1[0], v1[1]); w.w = cvt_pk_bf16(v1[2], v1[3]);
;                     *(LAS u32x4*)(my + fr * 144 + bj * 64 + fq * 16) = w;
;                 }
; #pragma unroll
;                 for (int hh = 0; hh < 2; ++hh) { const int row = (lane >> 3) + 8 * hh; const u32x4 x = *(const LAS u32x4*)(my + row * 144 + (lane & 7) * 16);
;                     *(u32x4*)(base + (size_t)(rowb + ai * 128 + wr * 64 + m * 16 + row) * ldc + colw) = x; }
.LBB0_300:
	v_cvt_pk_bf16_f32 v70, v70, v71
	v_cvt_pk_bf16_f32 v71, v72, v73
	v_cvt_pk_bf16_f32 v72, v66, v67
	s_nop 0
	v_cvt_pk_bf16_f32 v73, v68, v69
	ds_write_b128 v180, v[70:73] offset:64
	s_add_i32 s12, s6, 48
	ds_read_b128 v[66:69], v181
	v_add_u32_e32 v70, s12, v169
	v_ashrrev_i32_e32 v71, 31, v70
	v_mul_lo_u32 v72, s64, v71
	v_mul_lo_u32 v73, s65, v70
	v_mad_u64_u32 v[70:71], s[44:45], s64, v70, 0
	v_add3_u32 v71, v71, v72, v73
	v_lshl_add_u64 v[74:75], v[70:71], 1, v[122:123]
	ds_read_b128 v[70:73], v181 offset:1152
	s_waitcnt lgkmcnt(0)
	global_store_dwordx4 v[74:75], v[66:69], off sc0 sc1
	s_and_b64 vcc, exec, s[0:1]
	s_nop 0
	v_add_u32_e32 v66, s12, v172
	v_ashrrev_i32_e32 v67, 31, v66
	v_mul_lo_u32 v68, s64, v67
	v_mul_lo_u32 v69, s65, v66
	v_mad_u64_u32 v[66:67], s[44:45], s64, v66, 0
	v_add3_u32 v67, v67, v68, v69
	v_lshl_add_u64 v[66:67], v[66:67], 1, v[122:123]
	global_store_dwordx4 v[66:67], v[70:73], off sc0 sc1
	s_cbranch_vccnz .LBB0_302
	s_add_i32 s12, s79, s84
	s_lshl_b32 s12, s12, 1
	s_and_b32 s12, s12, 0x1f80
	v_lshl_add_u64 v[70:71], v[144:145], 0, s[12:13]
	global_load_dwordx4 v[66:69], v[70:71], off
	s_nop 0
	global_load_dwordx4 v[70:73], v[70:71], off offset:16
	s_waitcnt vmcnt(0)
	v_mov_b32_e32 v74, v66
	v_mul_f32_e32 v66, v64, v70
	v_mul_f32_e32 v76, v60, v71
	v_mul_f32_e32 v70, v60, v70
	v_mul_f32_e32 v78, v64, v71
	v_mov_b32_e32 v60, v65
	v_mov_b32_e32 v64, v61
	v_mov_b32_e32 v75, v68
	v_mov_b32_e32 v68, v67
	v_pk_mul_f32 v[60:61], v[60:61], v[72:73]
	v_pk_mul_f32 v[64:65], v[64:65], v[72:73]
	v_pk_mul_f32 v[80:81], v[58:59], v[68:69]
	v_pk_mul_f32 v[68:69], v[62:63], v[68:69]
	v_mov_b32_e32 v67, v60
	v_mov_b32_e32 v77, v61
	v_mov_b32_e32 v71, v64
	v_mov_b32_e32 v79, v65
	v_pk_fma_f32 v[62:63], v[62:63], v[74:75], v[80:81] neg_lo:[0,0,1] neg_hi:[0,0,1]
	v_pk_fma_f32 v[58:59], v[58:59], v[74:75], v[68:69]
	v_pk_add_f32 v[64:65], v[66:67], v[76:77] neg_lo:[0,1] neg_hi:[0,1]
	v_pk_add_f32 v[60:61], v[70:71], v[78:79]

; #define LAS __attribute__((address_space(3)))
; __device__ __forceinline__ unsigned cvt_pk_bf16(float lo, float hi) { unsigned r; asm volatile("v_cvt_pk_bf16_f32 %0, %1, %2" : "=v"(r) : "v"(lo), "v"(hi)); return r; }
;     __device__ __forceinline__ void operator()(const f32x4 (&acc)[2][2][4][2], const Unit& u, int wr, int wc, int fr, int fq) const {
;     ...
;             for (int m = 0; m < 4; ++m) {
;                 const int rl = ai * 128 + wr * 64 + m * 16 + fr;
;                 const int s = (lt * 256 + rl) & 4095, rpos = s >> 6, cpos = s & 63;
; #pragma unroll
;                 for (int bj = 0; bj < 2; ++bj) {
;                     f32x4 v0 = acc[ai][bj][m][0], v1 = acc[ai][bj][m][1];
;                     if (do_rope) {
;                         const int pos = bj ? cpos : rpos;
;                         const f32x4* cs = (const f32x4*)(rope + pos * 16 + 4 * fq);
;                         const f32x4 c01 = cs[0], c23 = cs[1];
;                         const float cc[4] = {c01[0], c01[2], c23[0], c23[2]}, sn[4] = {c01[1], c01[3], c23[1], c23[3]};
;                         f32x4 o0, o1;
; #pragma unroll
;                         for (int e = 0; e < 4; ++e) { o0[e] = v0[e] * cc[e] - v1[e] * sn[e]; o1[e] = v1[e] * cc[e] + v0[e] * sn[e]; }
;                         v0 = o0; v1 = o1;
;                     }
;                     u32x4 w; w.x = cvt_pk_bf16(v0[0], v0[1]); w.y = cvt_pk_bf16(v0[2], v0[3]); w.z = cvt_pk_bf16(v1[0], v1[1]); w.w = cvt_pk_bf16(v1[2], v1[3]);
;                     *(LAS u32x4*)(my + fr * 144 + bj * 64 + fq * 16) = w;
;                 }
; #pragma unroll
;                 for (int hh = 0; hh < 2; ++hh) { const int row = (lane >> 3) + 8 * hh; const u32x4 x = *(const LAS u32x4*)(my + row * 144 + (lane & 7) * 16);
;                     *(u32x4*)(base + (size_t)(rowb + ai * 128 + wr * 64 + m * 16 + row) * ldc + colw) = x; }
.LBB0_304:
	s_add_i32 s12, s6, 0x80
	v_cvt_pk_bf16_f32 v54, v54, v55
	v_cvt_pk_bf16_f32 v55, v56, v57
	v_cvt_pk_bf16_f32 v56, v50, v51
	v_cvt_pk_bf16_f32 v57, v52, v53
	ds_write_b128 v180, v[54:57] offset:64
	ds_read_b128 v[50:53], v181
	v_add_u32_e32 v54, s12, v169
	v_ashrrev_i32_e32 v55, 31, v54
	v_mul_lo_u32 v56, s64, v55
	v_mul_lo_u32 v57, s65, v54
	v_mad_u64_u32 v[54:55], s[44:45], s64, v54, 0
	v_add3_u32 v55, v55, v56, v57
	v_lshl_add_u64 v[58:59], v[54:55], 1, v[122:123]
	ds_read_b128 v[54:57], v181 offset:1152
	s_waitcnt lgkmcnt(0)
	global_store_dwordx4 v[58:59], v[50:53], off sc0 sc1
	s_and_b64 vcc, exec, s[0:1]
	s_nop 0
	v_add_u32_e32 v50, s12, v172
	v_ashrrev_i32_e32 v51, 31, v50
	v_mul_lo_u32 v52, s64, v51
	v_mul_lo_u32 v53, s65, v50
	v_mad_u64_u32 v[50:51], s[44:45], s64, v50, 0
	v_add3_u32 v51, v51, v52, v53
	v_lshl_add_u64 v[50:51], v[50:51], 1, v[122:123]
	global_store_dwordx4 v[50:51], v[54:57], off sc0 sc1
	s_cbranch_vccnz .LBB0_306
	v_add_lshl_u32 v50, s84, v173, 1
	v_and_b32_e32 v142, 0x1f80, v50
	v_lshl_add_u64 v[54:55], v[144:145], 0, v[142:143]
	global_load_dwordx4 v[50:53], v[54:55], off
	s_nop 0
	global_load_dwordx4 v[54:57], v[54:55], off offset:16
	s_waitcnt vmcnt(0)
	v_mov_b32_e32 v58, v50
	v_mul_f32_e32 v50, v48, v54
	v_mul_f32_e32 v60, v44, v55
	v_mul_f32_e32 v54, v44, v54
	v_mul_f32_e32 v62, v48, v55
	v_mov_b32_e32 v44, v49
	v_mov_b32_e32 v48, v45
	v_mov_b32_e32 v59, v52
	v_mov_b32_e32 v52, v51
	v_pk_mul_f32 v[44:45], v[44:45], v[56:57]
	v_pk_mul_f32 v[48:49], v[48:49], v[56:57]
	v_pk_mul_f32 v[64:65], v[42:43], v[52:53]
	v_pk_mul_f32 v[52:53], v[46:47], v[52:53]
	v_mov_b32_e32 v51, v44
	v_mov_b32_e32 v61, v45
	v_mov_b32_e32 v55, v48
	v_mov_b32_e32 v63, v49
	v_pk_fma_f32 v[46:47], v[46:47], v[58:59], v[64:65] neg_lo:[0,0,1] neg_hi:[0,0,1]
	v_pk_fma_f32 v[42:43], v[42:43], v[58:59], v[52:53]
	v_pk_add_f32 v[48:49], v[50:51], v[60:61] neg_lo:[0,1] neg_hi:[0,1]
	v_pk_add_f32 v[44:45], v[54:55], v[62:63]

; #define LAS __attribute__((address_space(3)))
; __device__ __forceinline__ unsigned cvt_pk_bf16(float lo, float hi) { unsigned r; asm volatile("v_cvt_pk_bf16_f32 %0, %1, %2" : "=v"(r) : "v"(lo), "v"(hi)); return r; }
;     __device__ __forceinline__ void operator()(const f32x4 (&acc)[2][2][4][2], const Unit& u, int wr, int wc, int fr, int fq) const {
;     ...
;             for (int m = 0; m < 4; ++m) {
;                 const int rl = ai * 128 + wr * 64 + m * 16 + fr;
;                 const int s = (lt * 256 + rl) & 4095, rpos = s >> 6, cpos = s & 63;
; #pragma unroll
;                 for (int bj = 0; bj < 2; ++bj) {
;                     f32x4 v0 = acc[ai][bj][m][0], v1 = acc[ai][bj][m][1];
;                     if (do_rope) {
;                         const int pos = bj ? cpos : rpos;
;                         const f32x4* cs = (const f32x4*)(rope + pos * 16 + 4 * fq);
;                         const f32x4 c01 = cs[0], c23 = cs[1];
;                         const float cc[4] = {c01[0], c01[2], c23[0], c23[2]}, sn[4] = {c01[1], c01[3], c23[1], c23[3]};
;                         f32x4 o0, o1;
; #pragma unroll
;                         for (int e = 0; e < 4; ++e) { o0[e] = v0[e] * cc[e] - v1[e] * sn[e]; o1[e] = v1[e] * cc[e] + v0[e] * sn[e]; }
;                         v0 = o0; v1 = o1;
;                     }
;                     u32x4 w; w.x = cvt_pk_bf16(v0[0], v0[1]); w.y = cvt_pk_bf16(v0[2], v0[3]); w.z = cvt_pk_bf16(v1[0], v1[1]); w.w = cvt_pk_bf16(v1[2], v1[3]);
;                     *(LAS u32x4*)(my + fr * 144 + bj * 64 + fq * 16) = w;
;                 }
; #pragma unroll
;                 for (int hh = 0; hh < 2; ++hh) { const int row = (lane >> 3) + 8 * hh; const u32x4 x = *(const LAS u32x4*)(my + row * 144 + (lane & 7) * 16);
;                     *(u32x4*)(base + (size_t)(rowb + ai * 128 + wr * 64 + m * 16 + row) * ldc + colw) = x; }
.LBB0_308:
	v_cvt_pk_bf16_f32 v38, v38, v39
	v_cvt_pk_bf16_f32 v39, v40, v41
	v_cvt_pk_bf16_f32 v40, v34, v35
	s_nop 0
	v_cvt_pk_bf16_f32 v41, v36, v37
	ds_write_b128 v180, v[38:41] offset:64
	s_add_i32 s12, s6, 0x90
	ds_read_b128 v[34:37], v181
	v_add_u32_e32 v38, s12, v169
	v_ashrrev_i32_e32 v39, 31, v38
	v_mul_lo_u32 v40, s64, v39
	v_mul_lo_u32 v41, s65, v38
	v_mad_u64_u32 v[38:39], s[44:45], s64, v38, 0
	v_add3_u32 v39, v39, v40, v41
	v_lshl_add_u64 v[42:43], v[38:39], 1, v[122:123]
	ds_read_b128 v[38:41], v181 offset:1152
	s_waitcnt lgkmcnt(0)
	global_store_dwordx4 v[42:43], v[34:37], off sc0 sc1
	s_and_b64 vcc, exec, s[0:1]
	s_nop 0
	v_add_u32_e32 v34, s12, v172
	v_ashrrev_i32_e32 v35, 31, v34
	v_mul_lo_u32 v36, s64, v35
	v_mul_lo_u32 v37, s65, v34
	v_mad_u64_u32 v[34:35], s[44:45], s64, v34, 0
	v_add3_u32 v35, v35, v36, v37
	v_lshl_add_u64 v[34:35], v[34:35], 1, v[122:123]
	global_store_dwordx4 v[34:35], v[38:41], off sc0 sc1
	s_cbranch_vccnz .LBB0_310
	v_add_lshl_u32 v34, s84, v174, 1
	v_and_b32_e32 v142, 0x1f80, v34
	v_lshl_add_u64 v[38:39], v[144:145], 0, v[142:143]
	global_load_dwordx4 v[34:37], v[38:39], off
	s_nop 0
	global_load_dwordx4 v[38:41], v[38:39], off offset:16
	s_waitcnt vmcnt(0)
	v_mov_b32_e32 v42, v34
	v_mul_f32_e32 v34, v32, v38
	v_mul_f32_e32 v44, v28, v39
	v_mul_f32_e32 v38, v28, v38
	v_mul_f32_e32 v46, v32, v39
	v_mov_b32_e32 v28, v33
	v_mov_b32_e32 v32, v29
	v_mov_b32_e32 v43, v36
	v_mov_b32_e32 v36, v35
	v_pk_mul_f32 v[28:29], v[28:29], v[40:41]
	v_pk_mul_f32 v[32:33], v[32:33], v[40:41]
	v_pk_mul_f32 v[48:49], v[26:27], v[36:37]
	v_pk_mul_f32 v[36:37], v[30:31], v[36:37]
	v_mov_b32_e32 v35, v28
	v_mov_b32_e32 v45, v29
	v_mov_b32_e32 v39, v32
	v_mov_b32_e32 v47, v33
	v_pk_fma_f32 v[30:31], v[30:31], v[42:43], v[48:49] neg_lo:[0,0,1] neg_hi:[0,0,1]
	v_pk_fma_f32 v[26:27], v[26:27], v[42:43], v[36:37]
	v_pk_add_f32 v[32:33], v[34:35], v[44:45] neg_lo:[0,1] neg_hi:[0,1]
	v_pk_add_f32 v[28:29], v[38:39], v[46:47]

; #define LAS __attribute__((address_space(3)))
; __device__ __forceinline__ unsigned cvt_pk_bf16(float lo, float hi) { unsigned r; asm volatile("v_cvt_pk_bf16_f32 %0, %1, %2" : "=v"(r) : "v"(lo), "v"(hi)); return r; }
;     __device__ __forceinline__ void operator()(const f32x4 (&acc)[2][2][4][2], const Unit& u, int wr, int wc, int fr, int fq) const {
;     ...
;             for (int m = 0; m < 4; ++m) {
;                 const int rl = ai * 128 + wr * 64 + m * 16 + fr;
;                 const int s = (lt * 256 + rl) & 4095, rpos = s >> 6, cpos = s & 63;
; #pragma unroll
;                 for (int bj = 0; bj < 2; ++bj) {
;                     f32x4 v0 = acc[ai][bj][m][0], v1 = acc[ai][bj][m][1];
;                     if (do_rope) {
;                         const int pos = bj ? cpos : rpos;
;                         const f32x4* cs = (const f32x4*)(rope + pos * 16 + 4 * fq);
;                         const f32x4 c01 = cs[0], c23 = cs[1];
;                         const float cc[4] = {c01[0], c01[2], c23[0], c23[2]}, sn[4] = {c01[1], c01[3], c23[1], c23[3]};
;                         f32x4 o0, o1;
; #pragma unroll
;                         for (int e = 0; e < 4; ++e) { o0[e] = v0[e] * cc[e] - v1[e] * sn[e]; o1[e] = v1[e] * cc[e] + v0[e] * sn[e]; }
;                         v0 = o0; v1 = o1;
;                     }
;                     u32x4 w; w.x = cvt_pk_bf16(v0[0], v0[1]); w.y = cvt_pk_bf16(v0[2], v0[3]); w.z = cvt_pk_bf16(v1[0], v1[1]); w.w = cvt_pk_bf16(v1[2], v1[3]);
;                     *(LAS u32x4*)(my + fr * 144 + bj * 64 + fq * 16) = w;
;                 }
; #pragma unroll
;                 for (int hh = 0; hh < 2; ++hh) { const int row = (lane >> 3) + 8 * hh; const u32x4 x = *(const LAS u32x4*)(my + row * 144 + (lane & 7) * 16);
;                     *(u32x4*)(base + (size_t)(rowb + ai * 128 + wr * 64 + m * 16 + row) * ldc + colw) = x; }
.LBB0_312:
	v_cvt_pk_bf16_f32 v22, v22, v23
	v_cvt_pk_bf16_f32 v23, v24, v25
	v_cvt_pk_bf16_f32 v24, v18, v19
	s_nop 0
	v_cvt_pk_bf16_f32 v25, v20, v21
	ds_write_b128 v180, v[22:25] offset:64
	s_add_i32 s12, s6, 0xa0
	ds_read_b128 v[18:21], v181
	v_add_u32_e32 v22, s12, v169
	v_ashrrev_i32_e32 v23, 31, v22
	v_mul_lo_u32 v24, s64, v23
	v_mul_lo_u32 v25, s65, v22
	v_mad_u64_u32 v[22:23], s[44:45], s64, v22, 0
	v_add3_u32 v23, v23, v24, v25
	v_lshl_add_u64 v[26:27], v[22:23], 1, v[122:123]
	ds_read_b128 v[22:25], v181 offset:1152
	s_waitcnt lgkmcnt(0)
	global_store_dwordx4 v[26:27], v[18:21], off sc0 sc1
	s_and_b64 vcc, exec, s[0:1]
	s_nop 0
	v_add_u32_e32 v18, s12, v172
	v_ashrrev_i32_e32 v19, 31, v18
	v_mul_lo_u32 v20, s64, v19
	v_mul_lo_u32 v21, s65, v18
	v_mad_u64_u32 v[18:19], s[44:45], s64, v18, 0
	v_add3_u32 v19, v19, v20, v21
	v_lshl_add_u64 v[18:19], v[18:19], 1, v[122:123]
	global_store_dwordx4 v[18:19], v[22:25], off sc0 sc1
	s_cbranch_vccnz .LBB0_314
	v_add_lshl_u32 v18, s84, v175, 1
	v_and_b32_e32 v142, 0x1f80, v18
	v_lshl_add_u64 v[22:23], v[144:145], 0, v[142:143]
	global_load_dwordx4 v[18:21], v[22:23], off
	s_nop 0
	global_load_dwordx4 v[22:25], v[22:23], off offset:16
	s_waitcnt vmcnt(0)
	v_mov_b32_e32 v26, v18
	v_mul_f32_e32 v18, v16, v22
	v_mul_f32_e32 v28, v12, v23
	v_mul_f32_e32 v22, v12, v22
	v_mul_f32_e32 v30, v16, v23
	v_mov_b32_e32 v12, v17
	v_mov_b32_e32 v16, v13
	v_mov_b32_e32 v27, v20
	v_mov_b32_e32 v20, v19
	v_pk_mul_f32 v[12:13], v[12:13], v[24:25]
	v_pk_mul_f32 v[16:17], v[16:17], v[24:25]
	v_pk_mul_f32 v[32:33], v[10:11], v[20:21]
	v_pk_mul_f32 v[20:21], v[14:15], v[20:21]
	v_mov_b32_e32 v19, v12
	v_mov_b32_e32 v29, v13
	v_mov_b32_e32 v23, v16
	v_mov_b32_e32 v31, v17
	v_pk_fma_f32 v[14:15], v[14:15], v[26:27], v[32:33] neg_lo:[0,0,1] neg_hi:[0,0,1]
	v_pk_fma_f32 v[10:11], v[10:11], v[26:27], v[20:21]
	v_pk_add_f32 v[16:17], v[18:19], v[28:29] neg_lo:[0,1] neg_hi:[0,1]
	v_pk_add_f32 v[12:13], v[22:23], v[30:31]

; #define LAS __attribute__((address_space(3)))
; __device__ __forceinline__ unsigned cvt_pk_bf16(float lo, float hi) { unsigned r; asm volatile("v_cvt_pk_bf16_f32 %0, %1, %2" : "=v"(r) : "v"(lo), "v"(hi)); return r; }
; template <class E> __device__ __forceinline__ bool epi_keep(const Unit& u) { return EpiKeep<E>::get(u); }
; #define PG8_BAR __builtin_amdgcn_s_barrier()
; template <class Epi, class Sched, bool GATHER, bool F8 = false>
; __device__ __forceinline__ void gemm_phase(LAS unsigned char* lds, const int K, const Sched& S, const Epi& E) {
;     ...
;         if (!has_next) break;
;         if constexpr (EpiInit<Epi>::value) E.init(acc, pre);
;         else if (!epi_keep<Epi>(cur))
; #pragma unroll
;         for (int a = 0; a < 2; ++a)
; #pragma unroll
;             for (int b = 0; b < 2; ++b)
; #pragma unroll
;                 for (int m = 0; m < 4; ++m)
; #pragma unroll
;                     for (int n = 0; n < 2; ++n) acc[a][b][m][n] = (f32x4){0.f, 0.f, 0.f, 0.f};
;         cur = nxt; cA = nA; cB = nB; ++ui;
;         if constexpr (GATHER) {
; #pragma unroll
;             for (int h = 0; h < 2; ++h)
; #pragma unroll
;                 for (int i = 0; i < 2; ++i) vA[h][i] = vN[h][i];
;         }
;         if (wr == 1) PG8_BAR;
;     __device__ __forceinline__ void operator()(const f32x4 (&acc)[2][2][4][2], const Unit& u, int wr, int wc, int fr, int fq) const {
;     ...
;                     u32x4 w; w.x = cvt_pk_bf16(v0[0], v0[1]); w.y = cvt_pk_bf16(v0[2], v0[3]); w.z = cvt_pk_bf16(v1[0], v1[1]); w.w = cvt_pk_bf16(v1[2], v1[3]);
;                     *(LAS u32x4*)(my + fr * 144 + bj * 64 + fq * 16) = w;
;                 }
; #pragma unroll
;                 for (int hh = 0; hh < 2; ++hh) { const int row = (lane >> 3) + 8 * hh; const u32x4 x = *(const LAS u32x4*)(my + row * 144 + (lane & 7) * 16);
;                     *(u32x4*)(base + (size_t)(rowb + ai * 128 + wr * 64 + m * 16 + row) * ldc + colw) = x; }
.LBB0_316:
	v_cvt_pk_bf16_f32 v6, v6, v7
	v_cvt_pk_bf16_f32 v7, v8, v9
	v_cvt_pk_bf16_f32 v8, v2, v3
	s_nop 0
	v_cvt_pk_bf16_f32 v9, v4, v5
	ds_write_b128 v180, v[6:9] offset:64
	s_addk_i32 s6, 0xb0
	ds_read_b128 v[2:5], v181
	v_add_u32_e32 v6, s6, v169
	v_ashrrev_i32_e32 v7, 31, v6
	v_mul_lo_u32 v8, s64, v7
	v_mul_lo_u32 v9, s65, v6
	v_mad_u64_u32 v[6:7], s[0:1], s64, v6, 0
	v_add3_u32 v7, v7, v8, v9
	v_lshl_add_u64 v[10:11], v[6:7], 1, v[122:123]
	ds_read_b128 v[6:9], v181 offset:1152
	s_waitcnt lgkmcnt(0)
	global_store_dwordx4 v[10:11], v[2:5], off sc0 sc1
	s_andn2_b64 vcc, exec, s[46:47]
	s_nop 0
	v_add_u32_e32 v2, s6, v172
	v_ashrrev_i32_e32 v3, 31, v2
	v_mul_lo_u32 v4, s64, v3
	v_mul_lo_u32 v5, s65, v2
	v_mad_u64_u32 v[2:3], s[0:1], s64, v2, 0
	v_add3_u32 v3, v3, v4, v5
	v_lshl_add_u64 v[2:3], v[2:3], 1, v[122:123]
	s_mov_b64 s[0:1], -1
	global_store_dwordx4 v[2:3], v[6:9], off sc0 sc1
	s_cbranch_vccnz .LBB0_257
	s_andn2_b64 vcc, exec, s[16:17]
	s_cbranch_vccnz .LBB0_256
	s_barrier
	s_branch .LBB0_256

; #define LAS __attribute__((address_space(3)))
; __device__ __forceinline__ unsigned cvt_pk_bf16(float lo, float hi) { unsigned r; asm volatile("v_cvt_pk_bf16_f32 %0, %1, %2" : "=v"(r) : "v"(lo), "v"(hi)); return r; }
;     __device__ __forceinline__ void operator()(const f32x4 (&acc)[2][2][4][2], const Unit& u, int wr, int wc, int fr, int fq) const {
;     ...
; #pragma unroll
;         for (int ai = 0; ai < 2; ++ai)
; #pragma unroll
;             for (int m = 0; m < 4; ++m) {
; #pragma unroll
;                 for (int bj = 0; bj < 2; ++bj) { const f32x4 v0 = acc[ai][bj][m][0] * WSCALE_INV, v1 = acc[ai][bj][m][1] * WSCALE_INV;
;                     u32x4 w; w.x = cvt_pk_bf16(v0[0], v0[1]); w.y = cvt_pk_bf16(v0[2], v0[3]); w.z = cvt_pk_bf16(v1[0], v1[1]); w.w = cvt_pk_bf16(v1[2], v1[3]);
;                     *(LAS u32x4*)(my + fr * 144 + bj * 64 + fq * 16) = w; }
; #pragma unroll
;                 for (int hh = 0; hh < 2; ++hh) { const int row = (lane >> 3) + 8 * hh; const u32x4 x = *(const LAS u32x4*)(my + row * 144 + (lane & 7) * 16);
;                     *(u32x4*)(base + (size_t)(u.row0 + ai * 128 + wr * 64 + m * 16 + row) * ld) = x; }
;             }
.LBB0_354:
	s_and_b32 s39, s39, s90
	s_lshl_b32 s39, s39, 1
	v_pk_mul_f32 v[6:7], v[160:161], s[38:39] op_sel_hi:[1,0]
	v_pk_mul_f32 v[4:5], v[158:159], s[38:39] op_sel_hi:[1,0]
	v_pk_mul_f32 v[8:9], v[156:157], s[38:39] op_sel_hi:[1,0]
	v_pk_mul_f32 v[10:11], v[154:155], s[38:39] op_sel_hi:[1,0]
	v_cvt_pk_bf16_f32 v4, v4, v5
	v_cvt_pk_bf16_f32 v5, v6, v7
	s_add_u32 s48, s48, s39
	v_cvt_pk_bf16_f32 v6, v10, v11
	v_cvt_pk_bf16_f32 v7, v8, v9
	ds_write_b128 v209, v[4:7]
	v_pk_mul_f32 v[6:7], v[152:153], s[38:39] op_sel_hi:[1,0]
	v_pk_mul_f32 v[4:5], v[150:151], s[38:39] op_sel_hi:[1,0]
	v_pk_mul_f32 v[8:9], v[148:149], s[38:39] op_sel_hi:[1,0]
	v_pk_mul_f32 v[10:11], v[146:147], s[38:39] op_sel_hi:[1,0]
	v_cvt_pk_bf16_f32 v4, v4, v5
	v_cvt_pk_bf16_f32 v5, v6, v7
	s_addc_u32 s49, s49, 0
	v_cvt_pk_bf16_f32 v6, v10, v11
	v_cvt_pk_bf16_f32 v7, v8, v9
	ds_write_b128 v209, v[4:7] offset:64
	ds_read_b128 v[4:7], v210
	v_add_u32_e32 v8, s74, v191
	v_lshl_add_u64 v[2:3], s[48:49], 0, v[176:177]
	v_mad_i64_i32 v[8:9], s[48:49], s46, v8, 0
	v_lshl_add_u64 v[12:13], v[8:9], 1, v[2:3]
	ds_read_b128 v[8:11], v210 offset:1152
	s_waitcnt lgkmcnt(0)
	global_store_dwordx4 v[12:13], v[4:7], off sc0 sc1
	s_andn2_b64 vcc, exec, s[44:45]
	s_mov_b64 s[44:45], -1
	v_add_u32_e32 v4, s74, v192
	v_mad_i64_i32 v[4:5], s[48:49], s46, v4, 0
	v_lshl_add_u64 v[4:5], v[4:5], 1, v[2:3]
	global_store_dwordx4 v[4:5], v[8:11], off sc0 sc1
	v_pk_mul_f32 v[6:7], v[144:145], s[38:39] op_sel_hi:[1,0]
	v_pk_mul_f32 v[4:5], v[142:143], s[38:39] op_sel_hi:[1,0]
	v_pk_mul_f32 v[8:9], v[140:141], s[38:39] op_sel_hi:[1,0]
	v_pk_mul_f32 v[10:11], v[138:139], s[38:39] op_sel_hi:[1,0]
	v_cvt_pk_bf16_f32 v4, v4, v5
	v_cvt_pk_bf16_f32 v5, v6, v7
	s_nop 0
	v_cvt_pk_bf16_f32 v6, v10, v11
	v_cvt_pk_bf16_f32 v7, v8, v9
	ds_write_b128 v209, v[4:7]
	v_pk_mul_f32 v[6:7], v[136:137], s[38:39] op_sel_hi:[1,0]
	v_pk_mul_f32 v[4:5], v[134:135], s[38:39] op_sel_hi:[1,0]
	v_pk_mul_f32 v[8:9], v[132:133], s[38:39] op_sel_hi:[1,0]
	v_pk_mul_f32 v[10:11], v[130:131], s[38:39] op_sel_hi:[1,0]
	v_cvt_pk_bf16_f32 v4, v4, v5
	v_cvt_pk_bf16_f32 v5, v6, v7
	s_nop 0
	v_cvt_pk_bf16_f32 v6, v10, v11
	v_cvt_pk_bf16_f32 v7, v8, v9
	ds_write_b128 v209, v[4:7] offset:64
	ds_read_b128 v[4:7], v210
	v_add_u32_e32 v8, s74, v193
	v_mad_i64_i32 v[8:9], s[48:49], s46, v8, 0
	v_lshl_add_u64 v[12:13], v[8:9], 1, v[2:3]
	ds_read_b128 v[8:11], v210 offset:1152
	s_waitcnt lgkmcnt(0)
	global_store_dwordx4 v[12:13], v[4:7], off sc0 sc1
	s_nop 1
	v_add_u32_e32 v4, s74, v194
	v_mad_i64_i32 v[4:5], s[48:49], s46, v4, 0
	v_lshl_add_u64 v[4:5], v[4:5], 1, v[2:3]
	global_store_dwordx4 v[4:5], v[8:11], off sc0 sc1
	v_pk_mul_f32 v[6:7], v[128:129], s[38:39] op_sel_hi:[1,0]
	v_pk_mul_f32 v[4:5], v[126:127], s[38:39] op_sel_hi:[1,0]
	v_pk_mul_f32 v[8:9], v[124:125], s[38:39] op_sel_hi:[1,0]
	v_pk_mul_f32 v[10:11], v[122:123], s[38:39] op_sel_hi:[1,0]
	v_cvt_pk_bf16_f32 v4, v4, v5
	v_cvt_pk_bf16_f32 v5, v6, v7
	s_nop 0
	v_cvt_pk_bf16_f32 v6, v10, v11
	v_cvt_pk_bf16_f32 v7, v8, v9
	ds_write_b128 v209, v[4:7]
	v_pk_mul_f32 v[6:7], v[120:121], s[38:39] op_sel_hi:[1,0]
	v_pk_mul_f32 v[4:5], v[118:119], s[38:39] op_sel_hi:[1,0]
	v_pk_mul_f32 v[8:9], v[116:117], s[38:39] op_sel_hi:[1,0]
	v_pk_mul_f32 v[10:11], v[114:115], s[38:39] op_sel_hi:[1,0]
	v_cvt_pk_bf16_f32 v4, v4, v5
	v_cvt_pk_bf16_f32 v5, v6, v7
	s_nop 0
	v_cvt_pk_bf16_f32 v6, v10, v11
	v_cvt_pk_bf16_f32 v7, v8, v9
	ds_write_b128 v209, v[4:7] offset:64
	ds_read_b128 v[4:7], v210
	v_add_u32_e32 v8, s74, v195
	v_mad_i64_i32 v[8:9], s[48:49], s46, v8, 0
	v_lshl_add_u64 v[12:13], v[8:9], 1, v[2:3]
	ds_read_b128 v[8:11], v210 offset:1152
	s_waitcnt lgkmcnt(0)
	global_store_dwordx4 v[12:13], v[4:7], off sc0 sc1
	s_nop 1
	v_add_u32_e32 v4, s74, v196
	v_mad_i64_i32 v[4:5], s[48:49], s46, v4, 0
	v_lshl_add_u64 v[4:5], v[4:5], 1, v[2:3]
	global_store_dwordx4 v[4:5], v[8:11], off sc0 sc1
	v_pk_mul_f32 v[6:7], v[112:113], s[38:39] op_sel_hi:[1,0]
	v_pk_mul_f32 v[4:5], v[110:111], s[38:39] op_sel_hi:[1,0]
	v_pk_mul_f32 v[8:9], v[108:109], s[38:39] op_sel_hi:[1,0]
	v_pk_mul_f32 v[10:11], v[106:107], s[38:39] op_sel_hi:[1,0]
	v_cvt_pk_bf16_f32 v4, v4, v5
	v_cvt_pk_bf16_f32 v5, v6, v7
	s_nop 0
	v_cvt_pk_bf16_f32 v6, v10, v11
	v_cvt_pk_bf16_f32 v7, v8, v9
	ds_write_b128 v209, v[4:7]
	v_pk_mul_f32 v[6:7], v[104:105], s[38:39] op_sel_hi:[1,0]
	v_pk_mul_f32 v[4:5], v[102:103], s[38:39] op_sel_hi:[1,0]
	v_pk_mul_f32 v[8:9], v[100:101], s[38:39] op_sel_hi:[1,0]
	v_pk_mul_f32 v[10:11], v[98:99], s[38:39] op_sel_hi:[1,0]
	v_cvt_pk_bf16_f32 v4, v4, v5
	v_cvt_pk_bf16_f32 v5, v6, v7
	s_nop 0
	v_cvt_pk_bf16_f32 v6, v10, v11
	v_cvt_pk_bf16_f32 v7, v8, v9
	ds_write_b128 v209, v[4:7] offset:64
	ds_read_b128 v[4:7], v210
	v_add_u32_e32 v8, s74, v197
	v_mad_i64_i32 v[8:9], s[48:49], s46, v8, 0
	v_lshl_add_u64 v[12:13], v[8:9], 1, v[2:3]
	ds_read_b128 v[8:11], v210 offset:1152
	s_waitcnt lgkmcnt(0)
; #define LAS __attribute__((address_space(3)))
; __device__ __forceinline__ unsigned cvt_pk_bf16(float lo, float hi) { unsigned r; asm volatile("v_cvt_pk_bf16_f32 %0, %1, %2" : "=v"(r) : "v"(lo), "v"(hi)); return r; }
; template <class E> __device__ __forceinline__ bool epi_keep(const Unit& u) { return EpiKeep<E>::get(u); }
; #define PG8_BAR __builtin_amdgcn_s_barrier()
; template <class Epi, class Sched, bool GATHER, bool F8 = false>
; __device__ __forceinline__ void gemm_phase(LAS unsigned char* lds, const int K, const Sched& S, const Epi& E) {
;     ...
;         if (!has_next) break;
;         if constexpr (EpiInit<Epi>::value) E.init(acc, pre);
;         else if (!epi_keep<Epi>(cur))
; #pragma unroll
;         for (int a = 0; a < 2; ++a)
; #pragma unroll
;             for (int b = 0; b < 2; ++b)
; #pragma unroll
;                 for (int m = 0; m < 4; ++m)
; #pragma unroll
;                     for (int n = 0; n < 2; ++n) acc[a][b][m][n] = (f32x4){0.f, 0.f, 0.f, 0.f};
;         cur = nxt; cA = nA; cB = nB; ++ui;
;         if constexpr (GATHER) {
; #pragma unroll
;             for (int h = 0; h < 2; ++h)
; #pragma unroll
;                 for (int i = 0; i < 2; ++i) vA[h][i] = vN[h][i];
;         }
;         if (wr == 1) PG8_BAR;
;     __device__ __forceinline__ void operator()(const f32x4 (&acc)[2][2][4][2], const Unit& u, int wr, int wc, int fr, int fq) const {
;     ...
; #pragma unroll
;         for (int ai = 0; ai < 2; ++ai)
; #pragma unroll
;             for (int m = 0; m < 4; ++m) {
; #pragma unroll
;                 for (int bj = 0; bj < 2; ++bj) { const f32x4 v0 = acc[ai][bj][m][0] * WSCALE_INV, v1 = acc[ai][bj][m][1] * WSCALE_INV;
;                     u32x4 w; w.x = cvt_pk_bf16(v0[0], v0[1]); w.y = cvt_pk_bf16(v0[2], v0[3]); w.z = cvt_pk_bf16(v1[0], v1[1]); w.w = cvt_pk_bf16(v1[2], v1[3]);
;                     *(LAS u32x4*)(my + fr * 144 + bj * 64 + fq * 16) = w; }
; #pragma unroll
;                 for (int hh = 0; hh < 2; ++hh) { const int row = (lane >> 3) + 8 * hh; const u32x4 x = *(const LAS u32x4*)(my + row * 144 + (lane & 7) * 16);
;                     *(u32x4*)(base + (size_t)(u.row0 + ai * 128 + wr * 64 + m * 16 + row) * ld) = x; }
;             }
	global_store_dwordx4 v[12:13], v[4:7], off sc0 sc1
	s_nop 1
	v_add_u32_e32 v4, s74, v198
	v_mad_i64_i32 v[4:5], s[48:49], s46, v4, 0
	v_lshl_add_u64 v[4:5], v[4:5], 1, v[2:3]
	global_store_dwordx4 v[4:5], v[8:11], off sc0 sc1
	v_pk_mul_f32 v[6:7], v[96:97], s[38:39] op_sel_hi:[1,0]
	v_pk_mul_f32 v[4:5], v[94:95], s[38:39] op_sel_hi:[1,0]
	v_pk_mul_f32 v[8:9], v[92:93], s[38:39] op_sel_hi:[1,0]
	v_pk_mul_f32 v[10:11], v[90:91], s[38:39] op_sel_hi:[1,0]
	v_cvt_pk_bf16_f32 v4, v4, v5
	v_cvt_pk_bf16_f32 v5, v6, v7
	s_nop 0
	v_cvt_pk_bf16_f32 v6, v10, v11
	v_cvt_pk_bf16_f32 v7, v8, v9
	ds_write_b128 v209, v[4:7]
	v_pk_mul_f32 v[6:7], v[88:89], s[38:39] op_sel_hi:[1,0]
	v_pk_mul_f32 v[4:5], v[86:87], s[38:39] op_sel_hi:[1,0]
	v_pk_mul_f32 v[8:9], v[84:85], s[38:39] op_sel_hi:[1,0]
	v_pk_mul_f32 v[10:11], v[82:83], s[38:39] op_sel_hi:[1,0]
	v_cvt_pk_bf16_f32 v4, v4, v5
	v_cvt_pk_bf16_f32 v5, v6, v7
	s_nop 0
	v_cvt_pk_bf16_f32 v6, v10, v11
	v_cvt_pk_bf16_f32 v7, v8, v9
	ds_write_b128 v209, v[4:7] offset:64
	ds_read_b128 v[4:7], v210
	v_add_u32_e32 v8, s74, v199
	v_mad_i64_i32 v[8:9], s[48:49], s46, v8, 0
	v_lshl_add_u64 v[12:13], v[8:9], 1, v[2:3]
	ds_read_b128 v[8:11], v210 offset:1152
	s_waitcnt lgkmcnt(0)
	global_store_dwordx4 v[12:13], v[4:7], off sc0 sc1
	s_nop 1
	v_add_u32_e32 v4, s74, v200
	v_mad_i64_i32 v[4:5], s[48:49], s46, v4, 0
	v_lshl_add_u64 v[4:5], v[4:5], 1, v[2:3]
	global_store_dwordx4 v[4:5], v[8:11], off sc0 sc1
	v_pk_mul_f32 v[6:7], v[80:81], s[38:39] op_sel_hi:[1,0]
	v_pk_mul_f32 v[4:5], v[78:79], s[38:39] op_sel_hi:[1,0]
	v_pk_mul_f32 v[8:9], v[76:77], s[38:39] op_sel_hi:[1,0]
	v_pk_mul_f32 v[10:11], v[74:75], s[38:39] op_sel_hi:[1,0]
	v_cvt_pk_bf16_f32 v4, v4, v5
	v_cvt_pk_bf16_f32 v5, v6, v7
	s_nop 0
	v_cvt_pk_bf16_f32 v6, v10, v11
	v_cvt_pk_bf16_f32 v7, v8, v9
	ds_write_b128 v209, v[4:7]
	v_pk_mul_f32 v[6:7], v[72:73], s[38:39] op_sel_hi:[1,0]
	v_pk_mul_f32 v[4:5], v[70:71], s[38:39] op_sel_hi:[1,0]
	v_pk_mul_f32 v[8:9], v[68:69], s[38:39] op_sel_hi:[1,0]
	v_pk_mul_f32 v[10:11], v[66:67], s[38:39] op_sel_hi:[1,0]
	v_cvt_pk_bf16_f32 v4, v4, v5
	v_cvt_pk_bf16_f32 v5, v6, v7
	s_nop 0
	v_cvt_pk_bf16_f32 v6, v10, v11
	v_cvt_pk_bf16_f32 v7, v8, v9
	ds_write_b128 v209, v[4:7] offset:64
	ds_read_b128 v[4:7], v210
	v_add_u32_e32 v8, s74, v201
	v_mad_i64_i32 v[8:9], s[48:49], s46, v8, 0
	v_lshl_add_u64 v[12:13], v[8:9], 1, v[2:3]
	ds_read_b128 v[8:11], v210 offset:1152
	s_waitcnt lgkmcnt(0)
	global_store_dwordx4 v[12:13], v[4:7], off sc0 sc1
	s_nop 1
	v_add_u32_e32 v4, s74, v202
	v_mad_i64_i32 v[4:5], s[48:49], s46, v4, 0
	v_lshl_add_u64 v[4:5], v[4:5], 1, v[2:3]
	global_store_dwordx4 v[4:5], v[8:11], off sc0 sc1
	v_pk_mul_f32 v[6:7], v[64:65], s[38:39] op_sel_hi:[1,0]
	v_pk_mul_f32 v[4:5], v[62:63], s[38:39] op_sel_hi:[1,0]
	v_pk_mul_f32 v[8:9], v[60:61], s[38:39] op_sel_hi:[1,0]
	v_pk_mul_f32 v[10:11], v[58:59], s[38:39] op_sel_hi:[1,0]
	v_cvt_pk_bf16_f32 v4, v4, v5
	v_cvt_pk_bf16_f32 v5, v6, v7
	s_nop 0
	v_cvt_pk_bf16_f32 v6, v10, v11
	v_cvt_pk_bf16_f32 v7, v8, v9
	ds_write_b128 v209, v[4:7]
	v_pk_mul_f32 v[6:7], v[56:57], s[38:39] op_sel_hi:[1,0]
	v_pk_mul_f32 v[4:5], v[54:55], s[38:39] op_sel_hi:[1,0]
	v_pk_mul_f32 v[8:9], v[52:53], s[38:39] op_sel_hi:[1,0]
	v_pk_mul_f32 v[10:11], v[50:51], s[38:39] op_sel_hi:[1,0]
	v_cvt_pk_bf16_f32 v4, v4, v5
	v_cvt_pk_bf16_f32 v5, v6, v7
	s_nop 0
	v_cvt_pk_bf16_f32 v6, v10, v11
	v_cvt_pk_bf16_f32 v7, v8, v9
	ds_write_b128 v209, v[4:7] offset:64
	ds_read_b128 v[4:7], v210
	v_add_u32_e32 v8, s74, v203
	v_mad_i64_i32 v[8:9], s[48:49], s46, v8, 0
	v_lshl_add_u64 v[12:13], v[8:9], 1, v[2:3]
	ds_read_b128 v[8:11], v210 offset:1152
	s_waitcnt lgkmcnt(0)
	global_store_dwordx4 v[12:13], v[4:7], off sc0 sc1
	s_nop 1
	v_add_u32_e32 v4, s74, v204
	v_mad_i64_i32 v[4:5], s[48:49], s46, v4, 0
	v_lshl_add_u64 v[4:5], v[4:5], 1, v[2:3]
	global_store_dwordx4 v[4:5], v[8:11], off sc0 sc1
	v_pk_mul_f32 v[6:7], v[48:49], s[38:39] op_sel_hi:[1,0]
	v_pk_mul_f32 v[4:5], v[46:47], s[38:39] op_sel_hi:[1,0]
	v_pk_mul_f32 v[8:9], v[44:45], s[38:39] op_sel_hi:[1,0]
	v_pk_mul_f32 v[10:11], v[42:43], s[38:39] op_sel_hi:[1,0]
	v_cvt_pk_bf16_f32 v4, v4, v5
	v_cvt_pk_bf16_f32 v5, v6, v7
	s_nop 0
	v_cvt_pk_bf16_f32 v6, v10, v11
	v_cvt_pk_bf16_f32 v7, v8, v9
	ds_write_b128 v209, v[4:7]
	v_pk_mul_f32 v[6:7], v[40:41], s[38:39] op_sel_hi:[1,0]
	v_pk_mul_f32 v[4:5], v[38:39], s[38:39] op_sel_hi:[1,0]
	v_pk_mul_f32 v[8:9], v[36:37], s[38:39] op_sel_hi:[1,0]
	v_pk_mul_f32 v[10:11], v[34:35], s[38:39] op_sel_hi:[1,0]
	v_cvt_pk_bf16_f32 v4, v4, v5
	v_cvt_pk_bf16_f32 v5, v6, v7
	s_nop 0
	v_cvt_pk_bf16_f32 v6, v10, v11
	v_cvt_pk_bf16_f32 v7, v8, v9
	ds_write_b128 v209, v[4:7] offset:64
	ds_read_b128 v[4:7], v210
	v_add_u32_e32 v8, s74, v205
	v_mad_i64_i32 v[8:9], s[48:49], s46, v8, 0
	v_lshl_add_u64 v[12:13], v[8:9], 1, v[2:3]
	ds_read_b128 v[8:11], v210 offset:1152
	s_waitcnt lgkmcnt(0)
	global_store_dwordx4 v[12:13], v[4:7], off sc0 sc1
	s_nop 1
	v_add_u32_e32 v4, s74, v206
	v_mad_i64_i32 v[4:5], s[46:47], s46, v4, 0
	v_lshl_add_u64 v[2:3], v[4:5], 1, v[2:3]
	global_store_dwordx4 v[2:3], v[8:11], off sc0 sc1
	s_cbranch_vccnz .LBB0_337
	s_andn2_b64 vcc, exec, s[16:17]
	s_cbranch_vccnz .LBB0_336
	s_barrier
	s_branch .LBB0_336

; #define LAS __attribute__((address_space(3)))
;     __device__ __forceinline__ void operator()(f32x4 (&acc)[2][2][4][2], const Unit& u, int wr, int wc, int fr, int fq) const {
;     ...
;                 if (u.tag != 0) { const int row = lane >> 2; const u32x4 x = *(const LAS u32x4*)(my + row * 80 + (lane & 3) * 16);
;                     *(u32x4*)(YP8 + (size_t)(u.row0 + ai * 128 + wr * 64 + m * 16 + row) * DM + u.col0 + wc * 64 + 16 * (lane & 3)) = x; }
.LBB0_568:
	v_add_u32_e32 v156, s76, v166
	v_add_u32_e32 v5, v178, v150
	v_ashrrev_i32_e32 v157, 31, v156
	ds_read_b128 v[6:9], v5
	v_lshlrev_b64 v[156:157], 11, v[156:157]
	v_lshl_add_u64 v[156:157], s[24:25], 0, v[156:157]
	s_ashr_i32 s55, s54, 31
	v_lshl_add_u64 v[156:157], v[156:157], 0, s[54:55]
	v_lshl_add_u64 v[156:157], v[156:157], 0, s[12:13]
	v_lshl_add_u64 v[156:157], v[156:157], 0, v[150:151]
	s_waitcnt lgkmcnt(0)
	global_store_dwordx4 v[156:157], v[6:9], off sc0 sc1

; #define LAS __attribute__((address_space(3)))
;     __device__ __forceinline__ void operator()(f32x4 (&acc)[2][2][4][2], const Unit& u, int wr, int wc, int fr, int fq) const {
;     ...
;                 if (u.tag != 0) { const int row = lane >> 2; const u32x4 x = *(const LAS u32x4*)(my + row * 80 + (lane & 3) * 16);
;                     *(u32x4*)(YP8 + (size_t)(u.row0 + ai * 128 + wr * 64 + m * 16 + row) * DM + u.col0 + wc * 64 + 16 * (lane & 3)) = x; }
.LBB0_576:
	v_add_u32_e32 v156, s76, v169
	v_add_u32_e32 v5, v178, v150
	v_ashrrev_i32_e32 v157, 31, v156
	ds_read_b128 v[6:9], v5
	v_lshlrev_b64 v[156:157], 11, v[156:157]
	v_lshl_add_u64 v[156:157], s[24:25], 0, v[156:157]
	s_ashr_i32 s55, s54, 31
	v_lshl_add_u64 v[156:157], v[156:157], 0, s[54:55]
	v_lshl_add_u64 v[156:157], v[156:157], 0, s[12:13]
	v_lshl_add_u64 v[156:157], v[156:157], 0, v[150:151]
	s_waitcnt lgkmcnt(0)
	global_store_dwordx4 v[156:157], v[6:9], off sc0 sc1

; #define LAS __attribute__((address_space(3)))
;     __device__ __forceinline__ void operator()(f32x4 (&acc)[2][2][4][2], const Unit& u, int wr, int wc, int fr, int fq) const {
;     ...
;                 if (u.tag != 0) { const int row = lane >> 2; const u32x4 x = *(const LAS u32x4*)(my + row * 80 + (lane & 3) * 16);
;                     *(u32x4*)(YP8 + (size_t)(u.row0 + ai * 128 + wr * 64 + m * 16 + row) * DM + u.col0 + wc * 64 + 16 * (lane & 3)) = x; }
.LBB0_584:
	v_add_u32_e32 v156, s76, v172
	v_add_u32_e32 v5, v178, v150
	v_ashrrev_i32_e32 v157, 31, v156
	ds_read_b128 v[6:9], v5
	v_lshlrev_b64 v[156:157], 11, v[156:157]
	v_lshl_add_u64 v[156:157], s[24:25], 0, v[156:157]
	s_ashr_i32 s55, s54, 31
	v_lshl_add_u64 v[156:157], v[156:157], 0, s[54:55]
	v_lshl_add_u64 v[156:157], v[156:157], 0, s[12:13]
	v_lshl_add_u64 v[156:157], v[156:157], 0, v[150:151]
	s_waitcnt lgkmcnt(0)
	global_store_dwordx4 v[156:157], v[6:9], off sc0 sc1

; #define LAS __attribute__((address_space(3)))
;     __device__ __forceinline__ void operator()(f32x4 (&acc)[2][2][4][2], const Unit& u, int wr, int wc, int fr, int fq) const {
;     ...
;                 if (u.tag != 0) { const int row = lane >> 2; const u32x4 x = *(const LAS u32x4*)(my + row * 80 + (lane & 3) * 16);
;                     *(u32x4*)(YP8 + (size_t)(u.row0 + ai * 128 + wr * 64 + m * 16 + row) * DM + u.col0 + wc * 64 + 16 * (lane & 3)) = x; }
.LBB0_592:
	v_add_u32_e32 v156, s76, v174
	v_add_u32_e32 v5, v178, v150
	v_ashrrev_i32_e32 v157, 31, v156
	ds_read_b128 v[6:9], v5
	v_lshlrev_b64 v[156:157], 11, v[156:157]
	v_lshl_add_u64 v[156:157], s[24:25], 0, v[156:157]
	s_ashr_i32 s55, s54, 31
	v_lshl_add_u64 v[156:157], v[156:157], 0, s[54:55]
	v_lshl_add_u64 v[156:157], v[156:157], 0, s[12:13]
	v_lshl_add_u64 v[156:157], v[156:157], 0, v[150:151]
	s_waitcnt lgkmcnt(0)
	global_store_dwordx4 v[156:157], v[6:9], off sc0 sc1

; #define LAS __attribute__((address_space(3)))
;     __device__ __forceinline__ void operator()(f32x4 (&acc)[2][2][4][2], const Unit& u, int wr, int wc, int fr, int fq) const {
;     ...
;                 if (u.tag != 0) { const int row = lane >> 2; const u32x4 x = *(const LAS u32x4*)(my + row * 80 + (lane & 3) * 16);
;                     *(u32x4*)(YP8 + (size_t)(u.row0 + ai * 128 + wr * 64 + m * 16 + row) * DM + u.col0 + wc * 64 + 16 * (lane & 3)) = x; }
.LBB0_600:
	v_add_u32_e32 v156, s76, v175
	v_add_u32_e32 v5, v178, v150
	v_ashrrev_i32_e32 v157, 31, v156
	ds_read_b128 v[6:9], v5
	v_lshlrev_b64 v[156:157], 11, v[156:157]
	v_lshl_add_u64 v[156:157], s[24:25], 0, v[156:157]
	s_ashr_i32 s55, s54, 31
	v_lshl_add_u64 v[156:157], v[156:157], 0, s[54:55]
	v_lshl_add_u64 v[156:157], v[156:157], 0, s[12:13]
	v_lshl_add_u64 v[156:157], v[156:157], 0, v[150:151]
	s_waitcnt lgkmcnt(0)
	global_store_dwordx4 v[156:157], v[6:9], off sc0 sc1

; #define LAS __attribute__((address_space(3)))
;     __device__ __forceinline__ void operator()(f32x4 (&acc)[2][2][4][2], const Unit& u, int wr, int wc, int fr, int fq) const {
;     ...
;                 if (u.tag != 0) { const int row = lane >> 2; const u32x4 x = *(const LAS u32x4*)(my + row * 80 + (lane & 3) * 16);
;                     *(u32x4*)(YP8 + (size_t)(u.row0 + ai * 128 + wr * 64 + m * 16 + row) * DM + u.col0 + wc * 64 + 16 * (lane & 3)) = x; }
.LBB0_608:
	v_add_u32_e32 v156, s76, v176
	v_add_u32_e32 v5, v178, v150
	v_ashrrev_i32_e32 v157, 31, v156
	ds_read_b128 v[6:9], v5
	v_lshlrev_b64 v[156:157], 11, v[156:157]
	v_lshl_add_u64 v[156:157], s[24:25], 0, v[156:157]
	s_ashr_i32 s55, s54, 31
	v_lshl_add_u64 v[156:157], v[156:157], 0, s[54:55]
	v_lshl_add_u64 v[156:157], v[156:157], 0, s[12:13]
	v_lshl_add_u64 v[156:157], v[156:157], 0, v[150:151]
	s_waitcnt lgkmcnt(0)
	global_store_dwordx4 v[156:157], v[6:9], off sc0 sc1

; #define LAS __attribute__((address_space(3)))
;     __device__ __forceinline__ void operator()(f32x4 (&acc)[2][2][4][2], const Unit& u, int wr, int wc, int fr, int fq) const {
;     ...
;                 if (u.tag != 0) { const int row = lane >> 2; const u32x4 x = *(const LAS u32x4*)(my + row * 80 + (lane & 3) * 16);
;                     *(u32x4*)(YP8 + (size_t)(u.row0 + ai * 128 + wr * 64 + m * 16 + row) * DM + u.col0 + wc * 64 + 16 * (lane & 3)) = x; }
.LBB0_616:
	v_add_u32_e32 v156, s76, v177
	v_add_u32_e32 v5, v178, v150
	v_ashrrev_i32_e32 v157, 31, v156
	ds_read_b128 v[6:9], v5
	v_lshlrev_b64 v[156:157], 11, v[156:157]
	v_lshl_add_u64 v[156:157], s[24:25], 0, v[156:157]
	s_ashr_i32 s55, s54, 31
	v_lshl_add_u64 v[156:157], v[156:157], 0, s[54:55]
	v_lshl_add_u64 v[156:157], v[156:157], 0, s[12:13]
	v_lshl_add_u64 v[156:157], v[156:157], 0, v[150:151]
	s_waitcnt lgkmcnt(0)
	global_store_dwordx4 v[156:157], v[6:9], off sc0 sc1

; #define LAS __attribute__((address_space(3)))
; #define PG8_WAIT_V(n) asm volatile("s_waitcnt vmcnt(" #n ")" ::: "memory")
; #define PG8_BAR __builtin_amdgcn_s_barrier()
; template <class Epi, class Sched, bool GATHER, bool F8 = false>
; __device__ __forceinline__ void gemm_phase(LAS unsigned char* lds, const int K, const Sched& S, const Epi& E) {
;     ...
;     PG8_WAIT_V(0);
;     PG8_BAR;
;     __device__ __forceinline__ void operator()(f32x4 (&acc)[2][2][4][2], const Unit& u, int wr, int wc, int fr, int fq) const {
;     ...
;                 if (u.tag != 0) { const int row = lane >> 2; const u32x4 x = *(const LAS u32x4*)(my + row * 80 + (lane & 3) * 16);
;                     *(u32x4*)(YP8 + (size_t)(u.row0 + ai * 128 + wr * 64 + m * 16 + row) * DM + u.col0 + wc * 64 + 16 * (lane & 3)) = x; }
.LBB0_642:
	v_add_u32_e32 v1, s76, v166
	v_add_u32_e32 v6, 0xb0, v1
	v_add_u32_e32 v2, v178, v150
	v_ashrrev_i32_e32 v7, 31, v6
	ds_read_b128 v[2:5], v2
	v_lshlrev_b64 v[6:7], 11, v[6:7]
	v_lshl_add_u64 v[6:7], s[24:25], 0, v[6:7]
	s_ashr_i32 s55, s54, 31
	v_lshl_add_u64 v[6:7], v[6:7], 0, s[54:55]
	v_lshl_add_u64 v[6:7], v[6:7], 0, s[12:13]
	v_lshl_add_u64 v[6:7], v[6:7], 0, v[150:151]
	s_waitcnt lgkmcnt(0)
	global_store_dwordx4 v[6:7], v[2:5], off sc0 sc1
	s_waitcnt vmcnt(0)
	v_readlane_b32 s56, v255, 7
	s_barrier

; #define LAS __attribute__((address_space(3)))
; __device__ __forceinline__ unsigned cvt_pk_bf16(float lo, float hi) { unsigned r; asm volatile("v_cvt_pk_bf16_f32 %0, %1, %2" : "=v"(r) : "v"(lo), "v"(hi)); return r; }
; #define PG8_BAR __builtin_amdgcn_s_barrier()
; #define PG8_SCHED __builtin_amdgcn_sched_barrier(0)
; template <class Epi, class Sched, bool GATHER, bool F8 = false>
; __device__ __forceinline__ void gemm_phase(LAS unsigned char* lds, const int K, const Sched& S, const Epi& E) {
;     ...
;         if (wr == 0) PG8_BAR;
;         if constexpr (F8) { asm volatile("s_nop 15\n\ts_nop 15" ::: "memory"); PG8_SCHED; }
;     __device__ __forceinline__ void operator()(const f32x4 (&acc)[2][2][4][2], const Unit& u, int wr, int wc, int fr, int fq) const {
;         const int lane = threadIdx.x & 63, b = u.row0 >> 12; LAS unsigned char* my = scr + (threadIdx.x >> 6) * 2304;
;         const int col0 = u.col0 + wc * 64 + 8 * fq, colw = u.col0 + wc * 64 + 8 * (lane & 7);
;         const float* gm = mod + (size_t)b * 12288 + 4096 + col0;
;         f32x4 gv[2][2];
; #pragma unroll
;         for (int bj = 0; bj < 2; ++bj)
; #pragma unroll
;             for (int n = 0; n < 2; ++n) gv[bj][n] = *(const f32x4*)(gm + bj * 32 + 4 * n) * (WSCALE_INV * PSCALE_INV);
; #pragma unroll
;         for (int ai = 0; ai < 2; ++ai)
; #pragma unroll
;             for (int m = 0; m < 4; ++m) {
;                 const float* xr = x + (size_t)(u.row0 + ai * 128 + wr * 64 + m * 16 + fr) * DM + col0;
; #pragma unroll
;                 for (int bj = 0; bj < 2; ++bj) { const f32x4 x0 = __builtin_nontemporal_load((const f32x4*)(xr + bj * 32)), x1 = __builtin_nontemporal_load((const f32x4*)(xr + bj * 32 + 4));
;                     const f32x4 v0 = x0 * DN_ALPHA + gv[bj][0] * acc[ai][bj][m][0], v1 = x1 * DN_ALPHA + gv[bj][1] * acc[ai][bj][m][1];
;                     u32x4 w; w.x = cvt_pk_bf16(v0[0], v0[1]); w.y = cvt_pk_bf16(v0[2], v0[3]); w.z = cvt_pk_bf16(v1[0], v1[1]); w.w = cvt_pk_bf16(v1[2], v1[3]);
;                     *(LAS u32x4*)(my + fr * 144 + bj * 64 + fq * 16) = w; }
; #pragma unroll
;                 for (int hh = 0; hh < 2; ++hh) { const int row = (lane >> 3) + 8 * hh; const u32x4 xx = *(const LAS u32x4*)(my + row * 144 + (lane & 7) * 16);
;                     *(u32x4*)(ZB + (size_t)(u.row0 + ai * 128 + wr * 64 + m * 16 + row) * DM + colw) = xx; }
.LBB0_705:
	v_bfe_u32 v163, v0, 3, 3
	v_or_b32_e32 v184, 8, v163
	s_or_b32 s6, s7, 32
	s_or_b32 s1, s7, 16
	v_or_b32_e32 v187, s6, v163
	v_or_b32_e32 v191, s6, v184
	s_sext_i32_i8 s6, s12
	s_nop 15
	s_nop 15
	s_or_b32 s13, s7, 48
	s_add_i32 s16, s7, 0x80
	s_add_i32 s17, s7, 0x90
	s_add_i32 s20, s7, 0xa0
	s_add_i32 s21, s7, 0xb0
	s_lshl_b32 s24, s47, 6
	v_mul_u32_u24_e32 v185, 0x90, v190
	v_or_b32_e32 v186, s1, v163
	v_or_b32_e32 v190, s1, v184
	s_lshl_b32 s1, s0, 8
	s_lshl_b32 s6, s6, 8
	s_add_u32 s12, s82, 0x4a600000
	v_and_b32_e32 v28, 7, v0
	s_movk_i32 s3, 0x90
	v_or_b32_e32 v182, s7, v163
	v_or_b32_e32 v33, s13, v163
	v_or_b32_e32 v31, s16, v163
	v_or_b32_e32 v29, s17, v163
	v_or_b32_e32 v26, s20, v163
	v_or_b32_e32 v24, s21, v184
	v_lshrrev_b32_e32 v188, 6, v0
	v_or_b32_e32 v183, s7, v184
	v_or_b32_e32 v162, s13, v184
	v_or_b32_e32 v32, s16, v184
	v_or_b32_e32 v30, s17, v184
	v_or_b32_e32 v27, s20, v184
	v_or_b32_e32 v25, s21, v163
	s_addc_u32 s13, s83, 0
	s_ashr_i32 s0, s0, 4
	s_or_b32 s17, s6, s24
	v_lshl_or_b32 v2, v189, 3, s17
	s_mul_hi_i32 s7, s0, 0xc000
	s_mul_i32 s0, s0, 0xc000
	s_add_u32 s6, s82, s0
	v_ashrrev_i32_e32 v3, 31, v2
	v_add_u32_e32 v14, s1, v171
	s_addc_u32 s7, s83, s7
	v_lshlrev_b64 v[2:3], 2, v[2:3]
	v_ashrrev_i32_e32 v15, 31, v14
	v_lshl_add_u64 v[12:13], s[6:7], 0, v[2:3]
	s_mov_b32 s0, 0x104000
	v_lshlrev_b64 v[4:5], 13, v[14:15]
	s_mov_b64 s[6:7], 0x104000
	v_lshl_add_u64 v[4:5], s[36:37], 0, v[4:5]
	v_add_co_u32_e32 v16, vcc, s0, v12
	v_lshl_add_u64 v[168:169], v[4:5], 0, v[2:3]
	s_nop 0
	v_addc_co_u32_e32 v17, vcc, 0, v13, vcc
	v_lshl_add_u64 v[12:13], v[12:13], 0, s[6:7]
	global_load_dwordx4 v[4:7], v[168:169], off offset:16 nt
	global_load_dwordx4 v[8:11], v[168:169], off nt
	global_load_dwordx4 v[20:23], v[12:13], off offset:16
	s_mov_b32 s16, 0x3b000000
	global_load_dwordx4 v[16:19], v[16:17], off
	s_mov_b32 s0, 0x3f9837f0
	global_load_dwordx4 v[164:167], v[12:13], off offset:144
	global_load_dwordx4 v[172:175], v[12:13], off offset:128
	s_add_i32 s7, 0, 0x20000
	s_movk_i32 s6, 0x900
	v_mov_b32_e32 v15, s7
	v_mad_u32_u24 v15, v188, s6, v15
	v_add3_u32 v1, v15, v185, v1
	v_add_u32_e32 v32, s1, v32
	v_add_u32_e32 v30, s1, v30
	v_add_u32_e32 v26, s1, v26
	v_add_u32_e32 v24, s1, v24
	v_readlane_b32 s56, v255, 7
	s_waitcnt vmcnt(0)
	v_pk_mul_f32 v[180:181], v[6:7], s[0:1] op_sel_hi:[1,0]
	v_pk_mul_f32 v[176:177], v[10:11], s[0:1] op_sel_hi:[1,0]
	v_pk_mul_f32 v[178:179], v[8:9], s[0:1] op_sel_hi:[1,0]
	v_pk_mul_f32 v[4:5], v[4:5], s[0:1] op_sel_hi:[1,0]
	v_pk_mul_f32 v[10:11], v[18:19], s[16:17] op_sel_hi:[1,0]
	v_pk_mul_f32 v[12:13], v[16:17], s[16:17] op_sel_hi:[1,0]
	v_pk_mul_f32 v[6:7], v[22:23], s[16:17] op_sel_hi:[1,0]
	v_pk_mul_f32 v[8:9], v[20:21], s[16:17] op_sel_hi:[1,0]
	v_pk_fma_f32 v[16:17], v[160:161], v[10:11], v[176:177]
	v_pk_fma_f32 v[18:19], v[158:159], v[12:13], v[178:179]
	v_pk_fma_f32 v[20:21], v[156:157], v[6:7], v[180:181]
	v_pk_fma_f32 v[4:5], v[154:155], v[8:9], v[4:5]
	v_cvt_pk_bf16_f32 v154, v18, v19
	v_cvt_pk_bf16_f32 v155, v16, v17
	v_add_u32_e32 v16, s1, v183
	v_cvt_pk_bf16_f32 v156, v4, v5
	v_cvt_pk_bf16_f32 v157, v20, v21
	global_load_dwordx4 v[158:161], v[168:169], off offset:128 nt
	global_load_dwordx4 v[176:179], v[168:169], off offset:144 nt
	v_add_u32_e32 v4, s1, v182
	v_lshl_or_b32 v18, v28, 3, s17
	v_ashrrev_i32_e32 v5, 31, v4
	v_ashrrev_i32_e32 v17, 31, v16
	v_add_u32_e32 v20, 16, v14
	v_ashrrev_i32_e32 v19, 31, v18
	v_lshlrev_b64 v[4:5], 12, v[4:5]
	v_lshlrev_b64 v[16:17], 12, v[16:17]
	v_ashrrev_i32_e32 v21, 31, v20
	v_lshl_add_u64 v[22:23], s[12:13], 0, v[4:5]
	v_lshlrev_b64 v[4:5], 1, v[18:19]
	v_lshl_add_u64 v[168:169], s[12:13], 0, v[16:17]
	v_lshl_add_u32 v16, v28, 4, v15
	v_lshlrev_b64 v[180:181], 13, v[20:21]
	v_lshl_add_u64 v[182:183], v[22:23], 0, v[4:5]
	v_mad_u32_u24 v15, v163, s3, v16
	v_mad_u32_u24 v28, v184, s3, v16
	v_pk_mul_f32 v[16:17], v[174:175], s[16:17] op_sel_hi:[1,0]
	v_pk_mul_f32 v[20:21], v[166:167], s[16:17] op_sel_hi:[1,0]
	v_pk_mul_f32 v[22:23], v[164:165], s[16:17] op_sel_hi:[1,0]
	ds_write_b128 v1, v[154:157]
	v_pk_mul_f32 v[18:19], v[172:173], s[16:17] op_sel_hi:[1,0]
	s_waitcnt vmcnt(1)
	v_pk_mul_f32 v[154:155], v[160:161], s[0:1] op_sel_hi:[1,0]
	v_pk_mul_f32 v[156:157], v[158:159], s[0:1] op_sel_hi:[1,0]
	s_waitcnt vmcnt(0)
	v_pk_mul_f32 v[158:159], v[178:179], s[0:1] op_sel_hi:[1,0]
	v_pk_mul_f32 v[160:161], v[176:177], s[0:1] op_sel_hi:[1,0]
	v_pk_fma_f32 v[152:153], v[152:153], v[16:17], v[154:155]
	v_pk_fma_f32 v[154:155], v[148:149], v[20:21], v[158:159]
	v_pk_fma_f32 v[148:149], v[146:147], v[22:23], v[160:161]
	v_pk_fma_f32 v[150:151], v[150:151], v[18:19], v[156:157]
	v_lshl_add_u64 v[156:157], s[36:37], 0, v[180:181]
	v_cvt_pk_bf16_f32 v146, v150, v151
	v_cvt_pk_bf16_f32 v147, v152, v153
	v_cvt_pk_bf16_f32 v148, v148, v149
	v_cvt_pk_bf16_f32 v149, v154, v155
	ds_write_b128 v1, v[146:149] offset:64
	ds_read_b128 v[146:149], v15
	ds_read_b128 v[150:153], v28
	v_lshl_add_u64 v[154:155], v[168:169], 0, v[4:5]
	v_lshl_add_u64 v[156:157], v[156:157], 0, v[2:3]
	s_waitcnt lgkmcnt(1)
	global_store_dwordx4 v[182:183], v[146:149], off sc0 sc1
	s_waitcnt lgkmcnt(0)
	global_store_dwordx4 v[154:155], v[150:153], off sc0 sc1
	global_load_dwordx4 v[146:149], v[156:157], off nt
	s_nop 0
	global_load_dwordx4 v[150:153], v[156:157], off offset:16 nt
	v_add_u32_e32 v154, 32, v14
	v_ashrrev_i32_e32 v155, 31, v154
	v_lshlrev_b64 v[154:155], 13, v[154:155]
	s_waitcnt vmcnt(1)
	v_pk_mul_f32 v[148:149], v[148:149], s[0:1] op_sel_hi:[1,0]
	v_pk_mul_f32 v[146:147], v[146:147], s[0:1] op_sel_hi:[1,0]
	s_waitcnt vmcnt(0)
; #define LAS __attribute__((address_space(3)))
; __device__ __forceinline__ unsigned cvt_pk_bf16(float lo, float hi) { unsigned r; asm volatile("v_cvt_pk_bf16_f32 %0, %1, %2" : "=v"(r) : "v"(lo), "v"(hi)); return r; }
;     __device__ __forceinline__ void operator()(const f32x4 (&acc)[2][2][4][2], const Unit& u, int wr, int wc, int fr, int fq) const {
;     ...
;         for (int ai = 0; ai < 2; ++ai)
; #pragma unroll
;             for (int m = 0; m < 4; ++m) {
;                 const float* xr = x + (size_t)(u.row0 + ai * 128 + wr * 64 + m * 16 + fr) * DM + col0;
; #pragma unroll
;                 for (int bj = 0; bj < 2; ++bj) { const f32x4 x0 = __builtin_nontemporal_load((const f32x4*)(xr + bj * 32)), x1 = __builtin_nontemporal_load((const f32x4*)(xr + bj * 32 + 4));
;                     const f32x4 v0 = x0 * DN_ALPHA + gv[bj][0] * acc[ai][bj][m][0], v1 = x1 * DN_ALPHA + gv[bj][1] * acc[ai][bj][m][1];
;                     u32x4 w; w.x = cvt_pk_bf16(v0[0], v0[1]); w.y = cvt_pk_bf16(v0[2], v0[3]); w.z = cvt_pk_bf16(v1[0], v1[1]); w.w = cvt_pk_bf16(v1[2], v1[3]);
;                     *(LAS u32x4*)(my + fr * 144 + bj * 64 + fq * 16) = w; }
; #pragma unroll
;                 for (int hh = 0; hh < 2; ++hh) { const int row = (lane >> 3) + 8 * hh; const u32x4 xx = *(const LAS u32x4*)(my + row * 144 + (lane & 7) * 16);
;                     *(u32x4*)(ZB + (size_t)(u.row0 + ai * 128 + wr * 64 + m * 16 + row) * DM + colw) = xx; }
	v_pk_mul_f32 v[152:153], v[152:153], s[0:1] op_sel_hi:[1,0]
	v_pk_mul_f32 v[150:151], v[150:151], s[0:1] op_sel_hi:[1,0]
	v_pk_fma_f32 v[144:145], v[144:145], v[10:11], v[148:149]
	v_pk_fma_f32 v[142:143], v[142:143], v[12:13], v[146:147]
	v_pk_fma_f32 v[146:147], v[140:141], v[6:7], v[152:153]
	v_pk_fma_f32 v[140:141], v[138:139], v[8:9], v[150:151]
	v_cvt_pk_bf16_f32 v138, v142, v143
	v_cvt_pk_bf16_f32 v139, v144, v145
	v_add_u32_e32 v150, s1, v186
	v_cvt_pk_bf16_f32 v140, v140, v141
	v_cvt_pk_bf16_f32 v141, v146, v147
	global_load_dwordx4 v[142:145], v[156:157], off offset:128 nt
	global_load_dwordx4 v[146:149], v[156:157], off offset:144 nt
	ds_write_b128 v1, v[138:141]
	v_add_u32_e32 v152, s1, v190
	v_ashrrev_i32_e32 v151, 31, v150
	v_ashrrev_i32_e32 v153, 31, v152
	v_lshlrev_b64 v[150:151], 12, v[150:151]
	v_lshlrev_b64 v[152:153], 12, v[152:153]
	v_lshl_add_u64 v[150:151], s[12:13], 0, v[150:151]
	v_lshl_add_u64 v[152:153], s[12:13], 0, v[152:153]
	v_lshl_add_u64 v[150:151], v[150:151], 0, v[4:5]
	s_waitcnt vmcnt(1)
	v_pk_mul_f32 v[138:139], v[144:145], s[0:1] op_sel_hi:[1,0]
	v_pk_mul_f32 v[140:141], v[142:143], s[0:1] op_sel_hi:[1,0]
	s_waitcnt vmcnt(0)
	v_pk_mul_f32 v[142:143], v[148:149], s[0:1] op_sel_hi:[1,0]
	v_pk_mul_f32 v[144:145], v[146:147], s[0:1] op_sel_hi:[1,0]
	v_pk_fma_f32 v[136:137], v[136:137], v[16:17], v[138:139]
	v_pk_fma_f32 v[138:139], v[132:133], v[20:21], v[142:143]
	v_pk_fma_f32 v[132:133], v[130:131], v[22:23], v[144:145]
	v_pk_fma_f32 v[134:135], v[134:135], v[18:19], v[140:141]
	v_lshl_add_u64 v[140:141], s[36:37], 0, v[154:155]
	v_cvt_pk_bf16_f32 v130, v134, v135
	v_cvt_pk_bf16_f32 v131, v136, v137
	v_cvt_pk_bf16_f32 v132, v132, v133
	v_cvt_pk_bf16_f32 v133, v138, v139
	ds_write_b128 v1, v[130:133] offset:64
	ds_read_b128 v[130:133], v15
	ds_read_b128 v[134:137], v28
	v_lshl_add_u64 v[138:139], v[152:153], 0, v[4:5]
	v_lshl_add_u64 v[140:141], v[140:141], 0, v[2:3]
	s_waitcnt lgkmcnt(1)
	global_store_dwordx4 v[150:151], v[130:133], off sc0 sc1
	s_waitcnt lgkmcnt(0)
	global_store_dwordx4 v[138:139], v[134:137], off sc0 sc1
	global_load_dwordx4 v[130:133], v[140:141], off nt
	s_nop 0
	global_load_dwordx4 v[134:137], v[140:141], off offset:16 nt
	v_add_u32_e32 v138, 48, v14
	v_ashrrev_i32_e32 v139, 31, v138
	v_lshlrev_b64 v[138:139], 13, v[138:139]
	s_waitcnt vmcnt(1)
	v_pk_mul_f32 v[132:133], v[132:133], s[0:1] op_sel_hi:[1,0]
	v_pk_mul_f32 v[130:131], v[130:131], s[0:1] op_sel_hi:[1,0]
	s_waitcnt vmcnt(0)
	v_pk_mul_f32 v[136:137], v[136:137], s[0:1] op_sel_hi:[1,0]
	v_pk_mul_f32 v[134:135], v[134:135], s[0:1] op_sel_hi:[1,0]
	v_pk_fma_f32 v[128:129], v[128:129], v[10:11], v[132:133]
	v_pk_fma_f32 v[126:127], v[126:127], v[12:13], v[130:131]
	v_pk_fma_f32 v[130:131], v[124:125], v[6:7], v[136:137]
	v_pk_fma_f32 v[124:125], v[122:123], v[8:9], v[134:135]
	v_cvt_pk_bf16_f32 v122, v126, v127
	v_cvt_pk_bf16_f32 v123, v128, v129
	v_add_u32_e32 v134, s1, v187
	v_cvt_pk_bf16_f32 v124, v124, v125
	v_cvt_pk_bf16_f32 v125, v130, v131
	global_load_dwordx4 v[126:129], v[140:141], off offset:128 nt
	global_load_dwordx4 v[130:133], v[140:141], off offset:144 nt
	ds_write_b128 v1, v[122:125]
	v_add_u32_e32 v136, s1, v191
	v_ashrrev_i32_e32 v135, 31, v134
	v_ashrrev_i32_e32 v137, 31, v136
	v_lshlrev_b64 v[134:135], 12, v[134:135]
	v_lshlrev_b64 v[136:137], 12, v[136:137]
	v_lshl_add_u64 v[134:135], s[12:13], 0, v[134:135]
	v_lshl_add_u64 v[136:137], s[12:13], 0, v[136:137]
	v_lshl_add_u64 v[134:135], v[134:135], 0, v[4:5]
	s_waitcnt vmcnt(1)
	v_pk_mul_f32 v[122:123], v[128:129], s[0:1] op_sel_hi:[1,0]
	v_pk_mul_f32 v[124:125], v[126:127], s[0:1] op_sel_hi:[1,0]
	s_waitcnt vmcnt(0)
	v_pk_mul_f32 v[126:127], v[132:133], s[0:1] op_sel_hi:[1,0]
	v_pk_mul_f32 v[128:129], v[130:131], s[0:1] op_sel_hi:[1,0]
	v_pk_fma_f32 v[120:121], v[120:121], v[16:17], v[122:123]
	v_pk_fma_f32 v[122:123], v[116:117], v[20:21], v[126:127]
	v_pk_fma_f32 v[116:117], v[114:115], v[22:23], v[128:129]
	v_pk_fma_f32 v[118:119], v[118:119], v[18:19], v[124:125]
	v_lshl_add_u64 v[124:125], s[36:37], 0, v[138:139]
	v_cvt_pk_bf16_f32 v114, v118, v119
	v_cvt_pk_bf16_f32 v115, v120, v121
	v_cvt_pk_bf16_f32 v116, v116, v117
	v_cvt_pk_bf16_f32 v117, v122, v123
	ds_write_b128 v1, v[114:117] offset:64
	ds_read_b128 v[114:117], v15
	ds_read_b128 v[118:121], v28
	v_lshl_add_u64 v[122:123], v[136:137], 0, v[4:5]
	v_lshl_add_u64 v[124:125], v[124:125], 0, v[2:3]
	s_waitcnt lgkmcnt(1)
	global_store_dwordx4 v[134:135], v[114:117], off sc0 sc1
	s_waitcnt lgkmcnt(0)
	global_store_dwordx4 v[122:123], v[118:121], off sc0 sc1
	global_load_dwordx4 v[114:117], v[124:125], off nt
	s_nop 0
	global_load_dwordx4 v[118:121], v[124:125], off offset:16 nt
	v_add_u32_e32 v122, 0x80, v14
	v_ashrrev_i32_e32 v123, 31, v122
	v_lshlrev_b64 v[122:123], 13, v[122:123]
	s_waitcnt vmcnt(1)
	v_pk_mul_f32 v[116:117], v[116:117], s[0:1] op_sel_hi:[1,0]
	v_pk_mul_f32 v[114:115], v[114:115], s[0:1] op_sel_hi:[1,0]
	s_waitcnt vmcnt(0)
	v_pk_mul_f32 v[120:121], v[120:121], s[0:1] op_sel_hi:[1,0]
	v_pk_mul_f32 v[118:119], v[118:119], s[0:1] op_sel_hi:[1,0]
	v_pk_fma_f32 v[112:113], v[112:113], v[10:11], v[116:117]
	v_pk_fma_f32 v[110:111], v[110:111], v[12:13], v[114:115]
	v_pk_fma_f32 v[114:115], v[108:109], v[6:7], v[120:121]
	v_pk_fma_f32 v[108:109], v[106:107], v[8:9], v[118:119]
	v_cvt_pk_bf16_f32 v106, v110, v111
	v_cvt_pk_bf16_f32 v107, v112, v113
	v_add_u32_e32 v118, s1, v33
	v_cvt_pk_bf16_f32 v108, v108, v109
	v_cvt_pk_bf16_f32 v109, v114, v115
	global_load_dwordx4 v[110:113], v[124:125], off offset:128 nt
	global_load_dwordx4 v[114:117], v[124:125], off offset:144 nt
	ds_write_b128 v1, v[106:109]
	v_add_u32_e32 v120, s1, v162
	v_ashrrev_i32_e32 v119, 31, v118
	v_ashrrev_i32_e32 v121, 31, v120
	v_lshlrev_b64 v[118:119], 12, v[118:119]
	v_lshlrev_b64 v[120:121], 12, v[120:121]
	v_lshl_add_u64 v[118:119], s[12:13], 0, v[118:119]
	v_lshl_add_u64 v[120:121], s[12:13], 0, v[120:121]
	v_lshl_add_u64 v[118:119], v[118:119], 0, v[4:5]
	v_ashrrev_i32_e32 v33, 31, v32
	v_lshlrev_b64 v[32:33], 12, v[32:33]
	v_lshl_add_u64 v[32:33], s[12:13], 0, v[32:33]
	v_lshl_add_u64 v[32:33], v[32:33], 0, v[4:5]
	s_waitcnt vmcnt(1)
; #define LAS __attribute__((address_space(3)))
; __device__ __forceinline__ unsigned cvt_pk_bf16(float lo, float hi) { unsigned r; asm volatile("v_cvt_pk_bf16_f32 %0, %1, %2" : "=v"(r) : "v"(lo), "v"(hi)); return r; }
;     __device__ __forceinline__ void operator()(const f32x4 (&acc)[2][2][4][2], const Unit& u, int wr, int wc, int fr, int fq) const {
;     ...
;         for (int ai = 0; ai < 2; ++ai)
; #pragma unroll
;             for (int m = 0; m < 4; ++m) {
;                 const float* xr = x + (size_t)(u.row0 + ai * 128 + wr * 64 + m * 16 + fr) * DM + col0;
; #pragma unroll
;                 for (int bj = 0; bj < 2; ++bj) { const f32x4 x0 = __builtin_nontemporal_load((const f32x4*)(xr + bj * 32)), x1 = __builtin_nontemporal_load((const f32x4*)(xr + bj * 32 + 4));
;                     const f32x4 v0 = x0 * DN_ALPHA + gv[bj][0] * acc[ai][bj][m][0], v1 = x1 * DN_ALPHA + gv[bj][1] * acc[ai][bj][m][1];
;                     u32x4 w; w.x = cvt_pk_bf16(v0[0], v0[1]); w.y = cvt_pk_bf16(v0[2], v0[3]); w.z = cvt_pk_bf16(v1[0], v1[1]); w.w = cvt_pk_bf16(v1[2], v1[3]);
;                     *(LAS u32x4*)(my + fr * 144 + bj * 64 + fq * 16) = w; }
; #pragma unroll
;                 for (int hh = 0; hh < 2; ++hh) { const int row = (lane >> 3) + 8 * hh; const u32x4 xx = *(const LAS u32x4*)(my + row * 144 + (lane & 7) * 16);
;                     *(u32x4*)(ZB + (size_t)(u.row0 + ai * 128 + wr * 64 + m * 16 + row) * DM + colw) = xx; }
	v_pk_mul_f32 v[106:107], v[112:113], s[0:1] op_sel_hi:[1,0]
	v_pk_mul_f32 v[108:109], v[110:111], s[0:1] op_sel_hi:[1,0]
	s_waitcnt vmcnt(0)
	v_pk_mul_f32 v[110:111], v[116:117], s[0:1] op_sel_hi:[1,0]
	v_pk_mul_f32 v[112:113], v[114:115], s[0:1] op_sel_hi:[1,0]
	v_pk_fma_f32 v[104:105], v[104:105], v[16:17], v[106:107]
	v_pk_fma_f32 v[106:107], v[100:101], v[20:21], v[110:111]
	v_pk_fma_f32 v[100:101], v[98:99], v[22:23], v[112:113]
	v_pk_fma_f32 v[102:103], v[102:103], v[18:19], v[108:109]
	v_lshl_add_u64 v[108:109], s[36:37], 0, v[122:123]
	v_cvt_pk_bf16_f32 v98, v102, v103
	v_cvt_pk_bf16_f32 v99, v104, v105
	v_cvt_pk_bf16_f32 v100, v100, v101
	v_cvt_pk_bf16_f32 v101, v106, v107
	ds_write_b128 v1, v[98:101] offset:64
	ds_read_b128 v[98:101], v15
	ds_read_b128 v[102:105], v28
	v_lshl_add_u64 v[106:107], v[120:121], 0, v[4:5]
	v_lshl_add_u64 v[108:109], v[108:109], 0, v[2:3]
	s_waitcnt lgkmcnt(1)
	global_store_dwordx4 v[118:119], v[98:101], off sc0 sc1
	s_waitcnt lgkmcnt(0)
	global_store_dwordx4 v[106:107], v[102:105], off sc0 sc1
	global_load_dwordx4 v[98:101], v[108:109], off nt
	s_nop 0
	global_load_dwordx4 v[102:105], v[108:109], off offset:16 nt
	s_waitcnt vmcnt(1)
	v_pk_mul_f32 v[100:101], v[100:101], s[0:1] op_sel_hi:[1,0]
	v_pk_mul_f32 v[98:99], v[98:99], s[0:1] op_sel_hi:[1,0]
	s_waitcnt vmcnt(0)
	v_pk_mul_f32 v[104:105], v[104:105], s[0:1] op_sel_hi:[1,0]
	v_pk_mul_f32 v[102:103], v[102:103], s[0:1] op_sel_hi:[1,0]
	v_pk_fma_f32 v[96:97], v[96:97], v[10:11], v[100:101]
	v_pk_fma_f32 v[94:95], v[94:95], v[12:13], v[98:99]
	v_pk_fma_f32 v[98:99], v[92:93], v[6:7], v[104:105]
	v_pk_fma_f32 v[92:93], v[90:91], v[8:9], v[102:103]
	v_cvt_pk_bf16_f32 v90, v94, v95
	v_cvt_pk_bf16_f32 v91, v96, v97
	v_add_u32_e32 v102, s1, v31
	v_cvt_pk_bf16_f32 v92, v92, v93
	v_cvt_pk_bf16_f32 v93, v98, v99
	global_load_dwordx4 v[94:97], v[108:109], off offset:128 nt
	global_load_dwordx4 v[98:101], v[108:109], off offset:144 nt
	ds_write_b128 v1, v[90:93]
	v_ashrrev_i32_e32 v103, 31, v102
	v_add_u32_e32 v104, 0x90, v14
	v_lshlrev_b64 v[102:103], 12, v[102:103]
	v_ashrrev_i32_e32 v105, 31, v104
	v_lshl_add_u64 v[102:103], s[12:13], 0, v[102:103]
	v_lshlrev_b64 v[104:105], 13, v[104:105]
	v_lshl_add_u64 v[102:103], v[102:103], 0, v[4:5]
	v_ashrrev_i32_e32 v31, 31, v30
	v_lshlrev_b64 v[30:31], 12, v[30:31]
	s_waitcnt vmcnt(1)
	v_pk_mul_f32 v[90:91], v[96:97], s[0:1] op_sel_hi:[1,0]
	v_pk_mul_f32 v[92:93], v[94:95], s[0:1] op_sel_hi:[1,0]
	s_waitcnt vmcnt(0)
	v_pk_mul_f32 v[94:95], v[100:101], s[0:1] op_sel_hi:[1,0]
	v_pk_mul_f32 v[96:97], v[98:99], s[0:1] op_sel_hi:[1,0]
	v_pk_fma_f32 v[88:89], v[88:89], v[16:17], v[90:91]
	v_pk_fma_f32 v[90:91], v[84:85], v[20:21], v[94:95]
	v_pk_fma_f32 v[84:85], v[82:83], v[22:23], v[96:97]
	v_pk_fma_f32 v[86:87], v[86:87], v[18:19], v[92:93]
	s_nop 0
	v_cvt_pk_bf16_f32 v82, v86, v87
	v_cvt_pk_bf16_f32 v83, v88, v89
	v_cvt_pk_bf16_f32 v84, v84, v85
	v_cvt_pk_bf16_f32 v85, v90, v91
	ds_write_b128 v1, v[82:85] offset:64
	ds_read_b128 v[82:85], v15
	ds_read_b128 v[86:89], v28
	v_lshl_add_u64 v[90:91], s[36:37], 0, v[104:105]
	v_lshl_add_u64 v[90:91], v[90:91], 0, v[2:3]
	s_waitcnt lgkmcnt(1)
	global_store_dwordx4 v[102:103], v[82:85], off sc0 sc1
	s_waitcnt lgkmcnt(0)
	global_store_dwordx4 v[32:33], v[86:89], off sc0 sc1
	global_load_dwordx4 v[82:85], v[90:91], off nt
	s_nop 0
	global_load_dwordx4 v[86:89], v[90:91], off offset:16 nt
	s_waitcnt vmcnt(1)
	v_pk_mul_f32 v[32:33], v[84:85], s[0:1] op_sel_hi:[1,0]
	v_pk_mul_f32 v[82:83], v[82:83], s[0:1] op_sel_hi:[1,0]
	s_waitcnt vmcnt(0)
	v_pk_mul_f32 v[84:85], v[88:89], s[0:1] op_sel_hi:[1,0]
	v_pk_mul_f32 v[86:87], v[86:87], s[0:1] op_sel_hi:[1,0]
	v_pk_fma_f32 v[32:33], v[80:81], v[10:11], v[32:33]
	v_pk_fma_f32 v[78:79], v[78:79], v[12:13], v[82:83]
	v_pk_fma_f32 v[80:81], v[76:77], v[6:7], v[84:85]
	v_pk_fma_f32 v[76:77], v[74:75], v[8:9], v[86:87]
	v_cvt_pk_bf16_f32 v74, v78, v79
	v_cvt_pk_bf16_f32 v75, v32, v33
	v_add_u32_e32 v32, s1, v29
	v_cvt_pk_bf16_f32 v76, v76, v77
	v_cvt_pk_bf16_f32 v77, v80, v81
	global_load_dwordx4 v[78:81], v[90:91], off offset:128 nt
	global_load_dwordx4 v[82:85], v[90:91], off offset:144 nt
	v_ashrrev_i32_e32 v33, 31, v32
	v_lshlrev_b64 v[32:33], 12, v[32:33]
	v_lshl_add_u64 v[32:33], s[12:13], 0, v[32:33]
	v_lshl_add_u64 v[88:89], s[12:13], 0, v[30:31]
	v_lshl_add_u64 v[90:91], v[32:33], 0, v[4:5]
	ds_write_b128 v1, v[74:77]
	v_add_u32_e32 v86, 0xa0, v14
	v_ashrrev_i32_e32 v87, 31, v86
	v_lshlrev_b64 v[86:87], 13, v[86:87]
	s_waitcnt vmcnt(1)
	v_pk_mul_f32 v[30:31], v[80:81], s[0:1] op_sel_hi:[1,0]
	v_pk_mul_f32 v[32:33], v[78:79], s[0:1] op_sel_hi:[1,0]
	s_waitcnt vmcnt(0)
; #define LAS __attribute__((address_space(3)))
; __device__ __forceinline__ unsigned cvt_pk_bf16(float lo, float hi) { unsigned r; asm volatile("v_cvt_pk_bf16_f32 %0, %1, %2" : "=v"(r) : "v"(lo), "v"(hi)); return r; }
; #define PG8_WAIT_V(n) asm volatile("s_waitcnt vmcnt(" #n ")" ::: "memory")
; #define PG8_BAR __builtin_amdgcn_s_barrier()
; template <class Epi, class Sched, bool GATHER, bool F8 = false>
; __device__ __forceinline__ void gemm_phase(LAS unsigned char* lds, const int K, const Sched& S, const Epi& E) {
;     ...
;     PG8_WAIT_V(0);
;     PG8_BAR;
;     __device__ __forceinline__ void operator()(const f32x4 (&acc)[2][2][4][2], const Unit& u, int wr, int wc, int fr, int fq) const {
;     ...
;         for (int ai = 0; ai < 2; ++ai)
; #pragma unroll
;             for (int m = 0; m < 4; ++m) {
;                 const float* xr = x + (size_t)(u.row0 + ai * 128 + wr * 64 + m * 16 + fr) * DM + col0;
; #pragma unroll
;                 for (int bj = 0; bj < 2; ++bj) { const f32x4 x0 = __builtin_nontemporal_load((const f32x4*)(xr + bj * 32)), x1 = __builtin_nontemporal_load((const f32x4*)(xr + bj * 32 + 4));
;                     const f32x4 v0 = x0 * DN_ALPHA + gv[bj][0] * acc[ai][bj][m][0], v1 = x1 * DN_ALPHA + gv[bj][1] * acc[ai][bj][m][1];
;                     u32x4 w; w.x = cvt_pk_bf16(v0[0], v0[1]); w.y = cvt_pk_bf16(v0[2], v0[3]); w.z = cvt_pk_bf16(v1[0], v1[1]); w.w = cvt_pk_bf16(v1[2], v1[3]);
;                     *(LAS u32x4*)(my + fr * 144 + bj * 64 + fq * 16) = w; }
; #pragma unroll
;                 for (int hh = 0; hh < 2; ++hh) { const int row = (lane >> 3) + 8 * hh; const u32x4 xx = *(const LAS u32x4*)(my + row * 144 + (lane & 7) * 16);
;                     *(u32x4*)(ZB + (size_t)(u.row0 + ai * 128 + wr * 64 + m * 16 + row) * DM + colw) = xx; }
	v_pk_mul_f32 v[76:77], v[82:83], s[0:1] op_sel_hi:[1,0]
	v_pk_mul_f32 v[74:75], v[84:85], s[0:1] op_sel_hi:[1,0]
	v_pk_fma_f32 v[72:73], v[72:73], v[16:17], v[30:31]
	v_pk_fma_f32 v[30:31], v[70:71], v[18:19], v[32:33]
	v_pk_fma_f32 v[32:33], v[66:67], v[22:23], v[76:77]
	v_pk_fma_f32 v[68:69], v[68:69], v[20:21], v[74:75]
	v_cvt_pk_bf16_f32 v30, v30, v31
	v_cvt_pk_bf16_f32 v31, v72, v73
	v_cvt_pk_bf16_f32 v32, v32, v33
	v_lshl_add_u64 v[72:73], s[36:37], 0, v[86:87]
	v_cvt_pk_bf16_f32 v33, v68, v69
	ds_write_b128 v1, v[30:33] offset:64
	ds_read_b128 v[30:33], v15
	ds_read_b128 v[66:69], v28
	v_lshl_add_u64 v[70:71], v[88:89], 0, v[4:5]
	v_lshl_add_u64 v[72:73], v[72:73], 0, v[2:3]
	s_waitcnt lgkmcnt(1)
	global_store_dwordx4 v[90:91], v[30:33], off sc0 sc1
	s_waitcnt lgkmcnt(0)
	global_store_dwordx4 v[70:71], v[66:69], off sc0 sc1
	global_load_dwordx4 v[30:33], v[72:73], off nt
	s_nop 0
	global_load_dwordx4 v[66:69], v[72:73], off offset:16 nt
	s_waitcnt vmcnt(1)
	v_pk_mul_f32 v[32:33], v[32:33], s[0:1] op_sel_hi:[1,0]
	v_pk_mul_f32 v[30:31], v[30:31], s[0:1] op_sel_hi:[1,0]
	s_waitcnt vmcnt(0)
	v_pk_mul_f32 v[68:69], v[68:69], s[0:1] op_sel_hi:[1,0]
	v_pk_mul_f32 v[66:67], v[66:67], s[0:1] op_sel_hi:[1,0]
	v_pk_fma_f32 v[32:33], v[64:65], v[10:11], v[32:33]
	v_pk_fma_f32 v[30:31], v[62:63], v[12:13], v[30:31]
	v_pk_fma_f32 v[60:61], v[60:61], v[6:7], v[68:69]
	v_pk_fma_f32 v[58:59], v[58:59], v[8:9], v[66:67]
	v_cvt_pk_bf16_f32 v30, v30, v31
	v_cvt_pk_bf16_f32 v31, v32, v33
	v_add_u32_e32 v66, s1, v27
	v_cvt_pk_bf16_f32 v32, v58, v59
	v_cvt_pk_bf16_f32 v33, v60, v61
	global_load_dwordx4 v[58:61], v[72:73], off offset:128 nt
	global_load_dwordx4 v[62:65], v[72:73], off offset:144 nt
	ds_write_b128 v1, v[30:33]
	v_ashrrev_i32_e32 v27, 31, v26
	v_add_u32_e32 v68, 0xb0, v14
	v_ashrrev_i32_e32 v67, 31, v66
	v_lshlrev_b64 v[26:27], 12, v[26:27]
	v_ashrrev_i32_e32 v69, 31, v68
	v_lshlrev_b64 v[66:67], 12, v[66:67]
	v_lshl_add_u64 v[26:27], s[12:13], 0, v[26:27]
	v_lshlrev_b64 v[68:69], 13, v[68:69]
	v_lshl_add_u64 v[66:67], s[12:13], 0, v[66:67]
	v_lshl_add_u64 v[26:27], v[26:27], 0, v[4:5]
	s_waitcnt vmcnt(1)
	v_pk_mul_f32 v[30:31], v[60:61], s[0:1] op_sel_hi:[1,0]
	v_pk_mul_f32 v[32:33], v[58:59], s[0:1] op_sel_hi:[1,0]
	s_waitcnt vmcnt(0)
	v_pk_mul_f32 v[60:61], v[62:63], s[0:1] op_sel_hi:[1,0]
	v_pk_mul_f32 v[58:59], v[64:65], s[0:1] op_sel_hi:[1,0]
	v_pk_fma_f32 v[56:57], v[56:57], v[16:17], v[30:31]
	v_pk_fma_f32 v[30:31], v[54:55], v[18:19], v[32:33]
	v_pk_fma_f32 v[32:33], v[50:51], v[22:23], v[60:61]
	v_pk_fma_f32 v[52:53], v[52:53], v[20:21], v[58:59]
	v_cvt_pk_bf16_f32 v30, v30, v31
	v_cvt_pk_bf16_f32 v31, v56, v57
	v_cvt_pk_bf16_f32 v32, v32, v33
	v_lshl_add_u64 v[56:57], s[36:37], 0, v[68:69]
	v_cvt_pk_bf16_f32 v33, v52, v53
	ds_write_b128 v1, v[30:33] offset:64
	ds_read_b128 v[30:33], v15
	ds_read_b128 v[50:53], v28
	v_lshl_add_u64 v[54:55], v[66:67], 0, v[4:5]
	v_lshl_add_u64 v[2:3], v[56:57], 0, v[2:3]
	s_waitcnt lgkmcnt(1)
	global_store_dwordx4 v[26:27], v[30:33], off sc0 sc1
	s_waitcnt lgkmcnt(0)
	global_store_dwordx4 v[54:55], v[50:53], off sc0 sc1
	global_load_dwordx4 v[30:33], v[2:3], off nt
	s_nop 0
	global_load_dwordx4 v[50:53], v[2:3], off offset:16 nt
	s_waitcnt vmcnt(1)
	v_pk_mul_f32 v[26:27], v[32:33], s[0:1] op_sel_hi:[1,0]
	v_pk_mul_f32 v[30:31], v[30:31], s[0:1] op_sel_hi:[1,0]
	s_waitcnt vmcnt(0)
	v_pk_mul_f32 v[50:51], v[50:51], s[0:1] op_sel_hi:[1,0]
	v_pk_mul_f32 v[32:33], v[52:53], s[0:1] op_sel_hi:[1,0]
	v_pk_fma_f32 v[10:11], v[48:49], v[10:11], v[26:27]
	v_pk_fma_f32 v[12:13], v[46:47], v[12:13], v[30:31]
	v_pk_fma_f32 v[8:9], v[42:43], v[8:9], v[50:51]
	v_pk_fma_f32 v[26:27], v[44:45], v[6:7], v[32:33]
	v_cvt_pk_bf16_f32 v6, v12, v13
	v_cvt_pk_bf16_f32 v7, v10, v11
	v_cvt_pk_bf16_f32 v8, v8, v9
	s_nop 0
	v_cvt_pk_bf16_f32 v9, v26, v27
	global_load_dwordx4 v[10:13], v[2:3], off offset:128 nt
	global_load_dwordx4 v[30:33], v[2:3], off offset:144 nt
	ds_write_b128 v1, v[6:9]
	v_add_u32_e32 v2, s1, v25
	v_ashrrev_i32_e32 v3, 31, v2
	v_ashrrev_i32_e32 v25, 31, v24
	v_lshlrev_b64 v[2:3], 12, v[2:3]
	v_lshlrev_b64 v[24:25], 12, v[24:25]
	v_lshl_add_u64 v[2:3], s[12:13], 0, v[2:3]
	v_lshl_add_u64 v[2:3], v[2:3], 0, v[4:5]
	s_waitcnt vmcnt(1)
	v_pk_mul_f32 v[6:7], v[12:13], s[0:1] op_sel_hi:[1,0]
	v_pk_mul_f32 v[8:9], v[10:11], s[0:1] op_sel_hi:[1,0]
	s_waitcnt vmcnt(0)
	v_pk_mul_f32 v[12:13], v[30:31], s[0:1] op_sel_hi:[1,0]
	v_pk_mul_f32 v[10:11], v[32:33], s[0:1] op_sel_hi:[1,0]
	v_pk_fma_f32 v[16:17], v[40:41], v[16:17], v[6:7]
	v_pk_fma_f32 v[6:7], v[38:39], v[18:19], v[8:9]
	v_pk_fma_f32 v[8:9], v[34:35], v[22:23], v[12:13]
	v_pk_fma_f32 v[10:11], v[36:37], v[20:21], v[10:11]
	v_cvt_pk_bf16_f32 v6, v6, v7
	v_cvt_pk_bf16_f32 v7, v16, v17
	v_cvt_pk_bf16_f32 v8, v8, v9
	s_nop 0
	v_cvt_pk_bf16_f32 v9, v10, v11
	ds_write_b128 v1, v[6:9] offset:64
	ds_read_b128 v[6:9], v15
	ds_read_b128 v[10:13], v28
	v_lshl_add_u64 v[14:15], s[12:13], 0, v[24:25]
	v_lshl_add_u64 v[4:5], v[14:15], 0, v[4:5]
	s_waitcnt lgkmcnt(1)
	global_store_dwordx4 v[2:3], v[6:9], off sc0 sc1
	s_waitcnt lgkmcnt(0)
	global_store_dwordx4 v[4:5], v[10:13], off sc0 sc1
	s_waitcnt vmcnt(0)
	s_barrier

; #define LAS __attribute__((address_space(3)))
; __device__ __forceinline__ unsigned cvt_pk_bf16(float lo, float hi) { unsigned r; asm volatile("v_cvt_pk_bf16_f32 %0, %1, %2" : "=v"(r) : "v"(lo), "v"(hi)); return r; }
;     __device__ __forceinline__ Pre preload(const Unit& u, int wr, int wc, int fr, int fq) const {
;         const float* pb = bd + (size_t)u.tag * DM + u.col0 + wc * 64 + 8 * fq;
;         Pre p;
; #pragma unroll
;         for (int bj = 0; bj < 2; ++bj)
; #pragma unroll
;             for (int n = 0; n < 2; ++n) p.bv[bj][n] = *(const f32x4*)(pb + bj * 32 + 4 * n);
;     __device__ __forceinline__ void operator()(const f32x4 (&acc)[2][2][4][2], const Unit& u, int wr, int wc, int fr, int fq) const {
;         const int lane = threadIdx.x & 63; LAS unsigned char* my = scr + (threadIdx.x >> 6) * 2304;
;         const int colw = u.col0 + wc * 64 + 8 * (lane & 7);
; #pragma unroll
;         for (int ai = 0; ai < 2; ++ai)
; #pragma unroll
;             for (int m = 0; m < 4; ++m) {
; #pragma unroll
;                 for (int bj = 0; bj < 2; ++bj) { const f32x4 v0 = acc[ai][bj][m][0] * WSCALE_INV, v1 = acc[ai][bj][m][1] * WSCALE_INV;
;                     u32x4 w; w.x = cvt_pk_bf16(v0[0], v0[1]); w.y = cvt_pk_bf16(v0[2], v0[3]); w.z = cvt_pk_bf16(v1[0], v1[1]); w.w = cvt_pk_bf16(v1[2], v1[3]);
;                     *(LAS u32x4*)(my + fr * 144 + bj * 64 + fq * 16) = w; }
; #pragma unroll
;                 for (int hh = 0; hh < 2; ++hh) { const int row = (lane >> 3) + 8 * hh; const u32x4 x = *(const LAS u32x4*)(my + row * 144 + (lane & 7) * 16);
;                     *(u32x4*)(Y + (size_t)(u.row0 + ai * 128 + wr * 64 + m * 16 + row) * DM + colw) = x; }
.LBB0_1131:
	s_nop 15
	s_nop 15
	s_ashr_i32 s13, s12, 31
	s_lshl_b64 s[40:41], s[12:13], 13
	s_add_u32 s13, s26, s40
	s_addc_u32 s18, s27, s41
	s_ashr_i32 s1, s0, 31
	s_lshl_b64 s[40:41], s[0:1], 2
	s_add_u32 s1, s13, s40
	s_addc_u32 s13, s18, s41
	s_lshl_b32 s18, s50, 2
	s_add_u32 s40, s1, s18
	s_addc_u32 s41, s13, 0
	global_load_dwordx4 v[74:77], v168, s[40:41] offset:16
	global_load_dwordx4 v[78:81], v168, s[40:41]
	global_load_dwordx4 v[2:5], v168, s[40:41] offset:144
	global_load_dwordx4 v[6:9], v168, s[40:41] offset:128
	v_pk_mul_f32 v[144:145], v[144:145], s[24:25] op_sel_hi:[1,0]
	v_pk_mul_f32 v[142:143], v[142:143], s[24:25] op_sel_hi:[1,0]
	v_pk_mul_f32 v[174:175], v[140:141], s[24:25] op_sel_hi:[1,0]
	v_pk_mul_f32 v[140:141], v[138:139], s[24:25] op_sel_hi:[1,0]
	v_cvt_pk_bf16_f32 v138, v142, v143
	v_cvt_pk_bf16_f32 v139, v144, v145
	s_add_i32 s1, s64, s55
	v_cvt_pk_bf16_f32 v140, v140, v141
	v_cvt_pk_bf16_f32 v141, v174, v175
	ds_write_b128 v169, v[138:141]
	v_pk_mul_f32 v[138:139], v[132:133], s[24:25] op_sel_hi:[1,0]
	v_pk_mul_f32 v[132:133], v[130:131], s[24:25] op_sel_hi:[1,0]
	v_pk_mul_f32 v[136:137], v[136:137], s[24:25] op_sel_hi:[1,0]
	v_pk_mul_f32 v[134:135], v[134:135], s[24:25] op_sel_hi:[1,0]
	v_add_u32_e32 v172, s0, v164
	v_cvt_pk_bf16_f32 v130, v134, v135
	v_cvt_pk_bf16_f32 v131, v136, v137
	v_cvt_pk_bf16_f32 v132, v132, v133
	v_cvt_pk_bf16_f32 v133, v138, v139
	ds_write_b128 v169, v[130:133] offset:64
	ds_read_b128 v[132:135], v171
	v_add_u32_e32 v130, s1, v165
	v_ashrrev_i32_e32 v131, 31, v130
	v_ashrrev_i32_e32 v173, 31, v172
	v_lshlrev_b64 v[130:131], 12, v[130:131]
	v_lshl_add_u64 v[136:137], s[14:15], 0, v[130:131]
	v_lshlrev_b64 v[130:131], 1, v[172:173]
	v_lshl_add_u64 v[140:141], v[136:137], 0, v[130:131]
	ds_read_b128 v[136:139], v171 offset:1152
	s_waitcnt lgkmcnt(0)
	global_store_dwordx4 v[140:141], v[132:135], off sc0 sc1
	v_pk_mul_f32 v[128:129], v[128:129], s[24:25] op_sel_hi:[1,0]
	v_pk_mul_f32 v[126:127], v[126:127], s[24:25] op_sel_hi:[1,0]
	v_add_u32_e32 v132, s1, v166
	v_ashrrev_i32_e32 v133, 31, v132
	v_lshlrev_b64 v[132:133], 12, v[132:133]
	v_lshl_add_u64 v[132:133], s[14:15], 0, v[132:133]
	v_lshl_add_u64 v[132:133], v[132:133], 0, v[130:131]
	global_store_dwordx4 v[132:133], v[136:139], off sc0 sc1
	v_pk_mul_f32 v[132:133], v[124:125], s[24:25] op_sel_hi:[1,0]
	v_pk_mul_f32 v[124:125], v[122:123], s[24:25] op_sel_hi:[1,0]
	v_cvt_pk_bf16_f32 v122, v126, v127
	v_cvt_pk_bf16_f32 v123, v128, v129
	v_pk_mul_f32 v[120:121], v[120:121], s[24:25] op_sel_hi:[1,0]
	v_cvt_pk_bf16_f32 v124, v124, v125
	v_cvt_pk_bf16_f32 v125, v132, v133
	ds_write_b128 v169, v[122:125]
	v_pk_mul_f32 v[122:123], v[116:117], s[24:25] op_sel_hi:[1,0]
	v_pk_mul_f32 v[116:117], v[114:115], s[24:25] op_sel_hi:[1,0]
	v_pk_mul_f32 v[118:119], v[118:119], s[24:25] op_sel_hi:[1,0]
	s_add_i32 s13, s1, 16
	v_cvt_pk_bf16_f32 v114, v118, v119
	v_cvt_pk_bf16_f32 v115, v120, v121
	v_cvt_pk_bf16_f32 v116, v116, v117
	v_cvt_pk_bf16_f32 v117, v122, v123
	ds_write_b128 v169, v[114:117] offset:64
	ds_read_b128 v[114:117], v171
	v_add_u32_e32 v118, s13, v165
	v_ashrrev_i32_e32 v119, 31, v118
	v_lshlrev_b64 v[118:119], 12, v[118:119]
	v_lshl_add_u64 v[118:119], s[14:15], 0, v[118:119]
	v_lshl_add_u64 v[122:123], v[118:119], 0, v[130:131]
	ds_read_b128 v[118:121], v171 offset:1152
	s_waitcnt lgkmcnt(0)
	global_store_dwordx4 v[122:123], v[114:117], off sc0 sc1
	v_pk_mul_f32 v[112:113], v[112:113], s[24:25] op_sel_hi:[1,0]
	v_pk_mul_f32 v[110:111], v[110:111], s[24:25] op_sel_hi:[1,0]
	v_add_u32_e32 v114, s13, v166
	v_ashrrev_i32_e32 v115, 31, v114
	v_lshlrev_b64 v[114:115], 12, v[114:115]
	v_lshl_add_u64 v[114:115], s[14:15], 0, v[114:115]
	v_lshl_add_u64 v[114:115], v[114:115], 0, v[130:131]
	global_store_dwordx4 v[114:115], v[118:121], off sc0 sc1
	v_pk_mul_f32 v[114:115], v[108:109], s[24:25] op_sel_hi:[1,0]
	v_pk_mul_f32 v[108:109], v[106:107], s[24:25] op_sel_hi:[1,0]
	v_cvt_pk_bf16_f32 v106, v110, v111
	v_cvt_pk_bf16_f32 v107, v112, v113
	v_pk_mul_f32 v[104:105], v[104:105], s[24:25] op_sel_hi:[1,0]
	v_cvt_pk_bf16_f32 v108, v108, v109
	v_cvt_pk_bf16_f32 v109, v114, v115
	ds_write_b128 v169, v[106:109]
	v_pk_mul_f32 v[106:107], v[100:101], s[24:25] op_sel_hi:[1,0]
	v_pk_mul_f32 v[100:101], v[98:99], s[24:25] op_sel_hi:[1,0]
	v_pk_mul_f32 v[102:103], v[102:103], s[24:25] op_sel_hi:[1,0]
	s_add_i32 s13, s1, 32
	v_cvt_pk_bf16_f32 v98, v102, v103
	v_cvt_pk_bf16_f32 v99, v104, v105
	v_cvt_pk_bf16_f32 v100, v100, v101
	v_cvt_pk_bf16_f32 v101, v106, v107
	ds_write_b128 v169, v[98:101] offset:64
	ds_read_b128 v[98:101], v171
	v_add_u32_e32 v102, s13, v165
	v_ashrrev_i32_e32 v103, 31, v102
	v_lshlrev_b64 v[102:103], 12, v[102:103]
	v_lshl_add_u64 v[102:103], s[14:15], 0, v[102:103]
	v_lshl_add_u64 v[106:107], v[102:103], 0, v[130:131]
	ds_read_b128 v[102:105], v171 offset:1152
	s_waitcnt lgkmcnt(0)
	global_store_dwordx4 v[106:107], v[98:101], off sc0 sc1
	v_pk_mul_f32 v[96:97], v[96:97], s[24:25] op_sel_hi:[1,0]
	v_pk_mul_f32 v[94:95], v[94:95], s[24:25] op_sel_hi:[1,0]
	v_add_u32_e32 v98, s13, v166
	v_ashrrev_i32_e32 v99, 31, v98
	v_lshlrev_b64 v[98:99], 12, v[98:99]
	v_lshl_add_u64 v[98:99], s[14:15], 0, v[98:99]
	v_lshl_add_u64 v[98:99], v[98:99], 0, v[130:131]
	global_store_dwordx4 v[98:99], v[102:105], off sc0 sc1
	v_pk_mul_f32 v[98:99], v[92:93], s[24:25] op_sel_hi:[1,0]
	v_pk_mul_f32 v[92:93], v[90:91], s[24:25] op_sel_hi:[1,0]
	v_cvt_pk_bf16_f32 v90, v94, v95
	v_cvt_pk_bf16_f32 v91, v96, v97
	v_pk_mul_f32 v[88:89], v[88:89], s[24:25] op_sel_hi:[1,0]
	v_cvt_pk_bf16_f32 v92, v92, v93
	v_cvt_pk_bf16_f32 v93, v98, v99
	ds_write_b128 v169, v[90:93]
	v_pk_mul_f32 v[90:91], v[84:85], s[24:25] op_sel_hi:[1,0]
	v_pk_mul_f32 v[84:85], v[82:83], s[24:25] op_sel_hi:[1,0]
	v_pk_mul_f32 v[86:87], v[86:87], s[24:25] op_sel_hi:[1,0]
	s_add_i32 s13, s1, 48
	v_cvt_pk_bf16_f32 v82, v86, v87
	v_cvt_pk_bf16_f32 v83, v88, v89
	v_cvt_pk_bf16_f32 v84, v84, v85
	v_cvt_pk_bf16_f32 v85, v90, v91
	ds_write_b128 v169, v[82:85] offset:64
	ds_read_b128 v[82:85], v171
	v_add_u32_e32 v86, s13, v165
	v_ashrrev_i32_e32 v87, 31, v86
	v_lshlrev_b64 v[86:87], 12, v[86:87]
	v_lshl_add_u64 v[86:87], s[14:15], 0, v[86:87]
	v_lshl_add_u64 v[90:91], v[86:87], 0, v[130:131]
	ds_read_b128 v[86:89], v171 offset:1152
	s_waitcnt lgkmcnt(0)
; #define LAS __attribute__((address_space(3)))
; __device__ __forceinline__ unsigned cvt_pk_bf16(float lo, float hi) { unsigned r; asm volatile("v_cvt_pk_bf16_f32 %0, %1, %2" : "=v"(r) : "v"(lo), "v"(hi)); return r; }
; template <class E> __device__ __forceinline__ bool epi_keep(const Unit& u) { return EpiKeep<E>::get(u); }
; #define PG8_BAR __builtin_amdgcn_s_barrier()
; template <class Epi, class Sched, bool GATHER, bool F8 = false>
; __device__ __forceinline__ void gemm_phase(LAS unsigned char* lds, const int K, const Sched& S, const Epi& E) {
;     ...
;         if (!has_next) break;
;         if constexpr (EpiInit<Epi>::value) E.init(acc, pre);
;         else if (!epi_keep<Epi>(cur))
; #pragma unroll
;         for (int a = 0; a < 2; ++a)
; #pragma unroll
;             for (int b = 0; b < 2; ++b)
; #pragma unroll
;                 for (int m = 0; m < 4; ++m)
; #pragma unroll
;                     for (int n = 0; n < 2; ++n) acc[a][b][m][n] = (f32x4){0.f, 0.f, 0.f, 0.f};
;         cur = nxt; cA = nA; cB = nB; ++ui;
;         if constexpr (GATHER) {
; #pragma unroll
;             for (int h = 0; h < 2; ++h)
; #pragma unroll
;                 for (int i = 0; i < 2; ++i) vA[h][i] = vN[h][i];
;         }
;         if (wr == 1) PG8_BAR;
;     __device__ __forceinline__ void operator()(const f32x4 (&acc)[2][2][4][2], const Unit& u, int wr, int wc, int fr, int fq) const {
;         const int lane = threadIdx.x & 63; LAS unsigned char* my = scr + (threadIdx.x >> 6) * 2304;
;         const int colw = u.col0 + wc * 64 + 8 * (lane & 7);
; #pragma unroll
;         for (int ai = 0; ai < 2; ++ai)
; #pragma unroll
;             for (int m = 0; m < 4; ++m) {
; #pragma unroll
;                 for (int bj = 0; bj < 2; ++bj) { const f32x4 v0 = acc[ai][bj][m][0] * WSCALE_INV, v1 = acc[ai][bj][m][1] * WSCALE_INV;
;                     u32x4 w; w.x = cvt_pk_bf16(v0[0], v0[1]); w.y = cvt_pk_bf16(v0[2], v0[3]); w.z = cvt_pk_bf16(v1[0], v1[1]); w.w = cvt_pk_bf16(v1[2], v1[3]);
;                     *(LAS u32x4*)(my + fr * 144 + bj * 64 + fq * 16) = w; }
; #pragma unroll
;                 for (int hh = 0; hh < 2; ++hh) { const int row = (lane >> 3) + 8 * hh; const u32x4 x = *(const LAS u32x4*)(my + row * 144 + (lane & 7) * 16);
;                     *(u32x4*)(Y + (size_t)(u.row0 + ai * 128 + wr * 64 + m * 16 + row) * DM + colw) = x; }
	global_store_dwordx4 v[90:91], v[82:85], off sc0 sc1
	v_pk_mul_f32 v[72:73], v[72:73], s[24:25] op_sel_hi:[1,0]
	v_pk_mul_f32 v[70:71], v[70:71], s[24:25] op_sel_hi:[1,0]
	v_add_u32_e32 v82, s13, v166
	v_ashrrev_i32_e32 v83, 31, v82
	v_lshlrev_b64 v[82:83], 12, v[82:83]
	v_lshl_add_u64 v[82:83], s[14:15], 0, v[82:83]
	v_lshl_add_u64 v[82:83], v[82:83], 0, v[130:131]
	global_store_dwordx4 v[82:83], v[86:89], off sc0 sc1
	v_pk_mul_f32 v[82:83], v[68:69], s[24:25] op_sel_hi:[1,0]
	v_pk_mul_f32 v[68:69], v[66:67], s[24:25] op_sel_hi:[1,0]
	v_cvt_pk_bf16_f32 v66, v70, v71
	v_cvt_pk_bf16_f32 v67, v72, v73
	s_add_i32 s13, s1, 0x80
	v_cvt_pk_bf16_f32 v68, v68, v69
	v_cvt_pk_bf16_f32 v69, v82, v83
	ds_write_b128 v169, v[66:69]
	v_pk_mul_f32 v[66:67], v[60:61], s[24:25] op_sel_hi:[1,0]
	v_pk_mul_f32 v[60:61], v[58:59], s[24:25] op_sel_hi:[1,0]
	v_pk_mul_f32 v[64:65], v[64:65], s[24:25] op_sel_hi:[1,0]
	v_pk_mul_f32 v[62:63], v[62:63], s[24:25] op_sel_hi:[1,0]
	v_pk_mul_f32 v[56:57], v[56:57], s[24:25] op_sel_hi:[1,0]
	v_cvt_pk_bf16_f32 v58, v62, v63
	v_cvt_pk_bf16_f32 v59, v64, v65
	v_cvt_pk_bf16_f32 v60, v60, v61
	v_cvt_pk_bf16_f32 v61, v66, v67
	ds_write_b128 v169, v[58:61] offset:64
	ds_read_b128 v[58:61], v171
	v_add_u32_e32 v62, s13, v165
	v_ashrrev_i32_e32 v63, 31, v62
	v_lshlrev_b64 v[62:63], 12, v[62:63]
	v_lshl_add_u64 v[62:63], s[14:15], 0, v[62:63]
	v_lshl_add_u64 v[66:67], v[62:63], 0, v[130:131]
	ds_read_b128 v[62:65], v171 offset:1152
	s_waitcnt lgkmcnt(0)
	global_store_dwordx4 v[66:67], v[58:61], off sc0 sc1
	v_pk_mul_f32 v[54:55], v[54:55], s[24:25] op_sel_hi:[1,0]
	v_pk_mul_f32 v[48:49], v[48:49], s[24:25] op_sel_hi:[1,0]
	v_add_u32_e32 v58, s13, v166
	v_ashrrev_i32_e32 v59, 31, v58
	v_lshlrev_b64 v[58:59], 12, v[58:59]
	v_lshl_add_u64 v[58:59], s[14:15], 0, v[58:59]
	v_lshl_add_u64 v[58:59], v[58:59], 0, v[130:131]
	global_store_dwordx4 v[58:59], v[62:65], off sc0 sc1
	v_pk_mul_f32 v[58:59], v[52:53], s[24:25] op_sel_hi:[1,0]
	v_pk_mul_f32 v[52:53], v[50:51], s[24:25] op_sel_hi:[1,0]
	v_cvt_pk_bf16_f32 v50, v54, v55
	v_cvt_pk_bf16_f32 v51, v56, v57
	v_pk_mul_f32 v[46:47], v[46:47], s[24:25] op_sel_hi:[1,0]
	v_cvt_pk_bf16_f32 v52, v52, v53
	v_cvt_pk_bf16_f32 v53, v58, v59
	ds_write_b128 v169, v[50:53]
	v_pk_mul_f32 v[50:51], v[44:45], s[24:25] op_sel_hi:[1,0]
	v_pk_mul_f32 v[44:45], v[42:43], s[24:25] op_sel_hi:[1,0]
	v_cvt_pk_bf16_f32 v42, v46, v47
	v_cvt_pk_bf16_f32 v43, v48, v49
	s_add_i32 s13, s1, 0x90
	v_cvt_pk_bf16_f32 v44, v44, v45
	v_cvt_pk_bf16_f32 v45, v50, v51
	ds_write_b128 v169, v[42:45] offset:64
	ds_read_b128 v[42:45], v171
	v_add_u32_e32 v46, s13, v165
	v_ashrrev_i32_e32 v47, 31, v46
	v_lshlrev_b64 v[46:47], 12, v[46:47]
	v_lshl_add_u64 v[46:47], s[14:15], 0, v[46:47]
	v_lshl_add_u64 v[50:51], v[46:47], 0, v[130:131]
	ds_read_b128 v[46:49], v171 offset:1152
	s_waitcnt lgkmcnt(0)
	global_store_dwordx4 v[50:51], v[42:45], off sc0 sc1
	v_pk_mul_f32 v[40:41], v[40:41], s[24:25] op_sel_hi:[1,0]
	v_pk_mul_f32 v[38:39], v[38:39], s[24:25] op_sel_hi:[1,0]
	v_add_u32_e32 v42, s13, v166
	v_ashrrev_i32_e32 v43, 31, v42
	v_lshlrev_b64 v[42:43], 12, v[42:43]
	v_lshl_add_u64 v[42:43], s[14:15], 0, v[42:43]
	v_lshl_add_u64 v[42:43], v[42:43], 0, v[130:131]
	global_store_dwordx4 v[42:43], v[46:49], off sc0 sc1
	v_pk_mul_f32 v[42:43], v[36:37], s[24:25] op_sel_hi:[1,0]
	v_pk_mul_f32 v[36:37], v[34:35], s[24:25] op_sel_hi:[1,0]
	v_cvt_pk_bf16_f32 v34, v38, v39
	v_cvt_pk_bf16_f32 v35, v40, v41
	v_pk_mul_f32 v[32:33], v[32:33], s[24:25] op_sel_hi:[1,0]
	v_cvt_pk_bf16_f32 v36, v36, v37
	v_cvt_pk_bf16_f32 v37, v42, v43
	ds_write_b128 v169, v[34:37]
	v_pk_mul_f32 v[34:35], v[28:29], s[24:25] op_sel_hi:[1,0]
	v_pk_mul_f32 v[28:29], v[26:27], s[24:25] op_sel_hi:[1,0]
	v_pk_mul_f32 v[30:31], v[30:31], s[24:25] op_sel_hi:[1,0]
	s_add_i32 s13, s1, 0xa0
	v_cvt_pk_bf16_f32 v26, v30, v31
	v_cvt_pk_bf16_f32 v27, v32, v33
	v_cvt_pk_bf16_f32 v28, v28, v29
	v_cvt_pk_bf16_f32 v29, v34, v35
	ds_write_b128 v169, v[26:29] offset:64
	ds_read_b128 v[26:29], v171
	v_add_u32_e32 v30, s13, v165
	v_ashrrev_i32_e32 v31, 31, v30
	v_lshlrev_b64 v[30:31], 12, v[30:31]
	v_lshl_add_u64 v[30:31], s[14:15], 0, v[30:31]
	v_lshl_add_u64 v[34:35], v[30:31], 0, v[130:131]
	ds_read_b128 v[30:33], v171 offset:1152
	s_waitcnt lgkmcnt(0)
	global_store_dwordx4 v[34:35], v[26:29], off sc0 sc1
	v_pk_mul_f32 v[20:21], v[20:21], s[24:25] op_sel_hi:[1,0]
	v_pk_mul_f32 v[18:19], v[18:19], s[24:25] op_sel_hi:[1,0]
	v_add_u32_e32 v26, s13, v166
	v_ashrrev_i32_e32 v27, 31, v26
	v_lshlrev_b64 v[26:27], 12, v[26:27]
	v_lshl_add_u64 v[26:27], s[14:15], 0, v[26:27]
	v_lshl_add_u64 v[26:27], v[26:27], 0, v[130:131]
	v_pk_mul_f32 v[12:13], v[12:13], s[24:25] op_sel_hi:[1,0]
	v_pk_mul_f32 v[10:11], v[10:11], s[24:25] op_sel_hi:[1,0]
	global_store_dwordx4 v[26:27], v[30:33], off sc0 sc1
	v_pk_mul_f32 v[24:25], v[24:25], s[24:25] op_sel_hi:[1,0]
	v_pk_mul_f32 v[22:23], v[22:23], s[24:25] op_sel_hi:[1,0]
	v_cvt_pk_bf16_f32 v18, v18, v19
	v_cvt_pk_bf16_f32 v19, v20, v21
	v_pk_mul_f32 v[16:17], v[16:17], s[24:25] op_sel_hi:[1,0]
	v_cvt_pk_bf16_f32 v20, v22, v23
	v_cvt_pk_bf16_f32 v21, v24, v25
	ds_write_b128 v169, v[18:21]
	v_pk_mul_f32 v[14:15], v[14:15], s[24:25] op_sel_hi:[1,0]
	v_cvt_pk_bf16_f32 v10, v10, v11
	v_cvt_pk_bf16_f32 v11, v12, v13
	s_addk_i32 s1, 0xb0
	v_cvt_pk_bf16_f32 v12, v14, v15
	v_cvt_pk_bf16_f32 v13, v16, v17
	ds_write_b128 v169, v[10:13] offset:64
	ds_read_b128 v[10:13], v171
	v_add_u32_e32 v14, s1, v165
	v_ashrrev_i32_e32 v15, 31, v14
	v_lshlrev_b64 v[14:15], 12, v[14:15]
	v_lshl_add_u64 v[14:15], s[14:15], 0, v[14:15]
	v_lshl_add_u64 v[18:19], v[14:15], 0, v[130:131]
	ds_read_b128 v[14:17], v171 offset:1152
	s_waitcnt lgkmcnt(0)
	global_store_dwordx4 v[18:19], v[10:13], off sc0 sc1
	s_andn2_b64 vcc, exec, s[4:5]
	s_mov_b64 s[4:5], -1
	v_add_u32_e32 v10, s1, v166
	v_ashrrev_i32_e32 v11, 31, v10
	v_lshlrev_b64 v[10:11], 12, v[10:11]
	v_lshl_add_u64 v[10:11], s[14:15], 0, v[10:11]
	v_lshl_add_u64 v[10:11], v[10:11], 0, v[130:131]
	global_store_dwordx4 v[10:11], v[14:17], off sc0 sc1
	s_cbranch_vccnz .LBB0_1124
	s_andn2_b64 vcc, exec, s[2:3]
	s_cbranch_vccnz .LBB0_1123
	s_barrier
	s_branch .LBB0_1123
